# strategy T5: s_setprio 1/0 flips around the QK and PV MFMA clusters of both attention loops (no other change)
# speedup vs baseline: 1.0018x; 1.0018x over previous
; #define LAS __attribute__((address_space(3)))
; __device__ __forceinline__ void qkt(f32x16& p0, f32x16& p1, LAS const unsigned char* Ks, const bf16x8* qr, int r32, int hi) {
;     p0 = f32x16{}; p1 = f32x16{};
; #pragma unroll
;     for (int d0 = 0; d0 < 8; ++d0) { const int cb = (d0 * 16 + hi * 8) * 2;
;         const bf16x8 b0 = *(LAS const bf16x8*)(Ks + ATT_KSWZ(r32, cb));
;         const bf16x8 b1 = *(LAS const bf16x8*)(Ks + ATT_KSWZ(32 + r32, cb));
;         p0 = __builtin_amdgcn_mfma_f32_32x32x16_bf16(b0, qr[d0], p0, 0, 0, 0);
;         p1 = __builtin_amdgcn_mfma_f32_32x32x16_bf16(b1, qr[d0], p1, 0, 0, 0); }
; __device__ __forceinline__ void finishSM(f32x16& p0, f32x16& p1, float alpha, float& l_reg, bf16x8& pa0, bf16x8& pa1, bf16x8& pa2, bf16x8& pa3) {
; #pragma unroll
;     for (int r = 0; r < 16; ++r) p1[r] = __builtin_amdgcn_exp2f(p1[r]);
;     float ps = 0;
; #pragma unroll
;     for (int r = 0; r < 16; ++r) ps += p0[r];
; #pragma unroll
;     for (int r = 0; r < 16; ++r) ps += p1[r];
;     { auto rr = __builtin_amdgcn_permlane32_swap(__float_as_uint(ps), __float_as_uint(ps), false, false);
;       ps = __uint_as_float(rr[0]) + __uint_as_float(rr[1]); }
;     l_reg = l_reg * alpha + ps;
;     ...
;     ATT_PK4(p0, 0, pa0); ATT_PK4(p0, 8, pa1); ATT_PK4(p1, 0, pa2); ATT_PK4(p1, 8, pa3);
;     ...
; }
; template <int D0> __device__ __forceinline__ void pv_one(f32x16& od, LAS const unsigned char* vb, bf16x8 pa0, bf16x8 pa1, bf16x8 pa2, bf16x8 pa3) {
;     const s16x4 l0 = tr_read(vb + v_rd_off(D0, 0, 0)), h0 = tr_read(vb + v_rd_off(D0, 0, 1)), l1 = tr_read(vb + v_rd_off(D0, 1, 0)), h1 = tr_read(vb + v_rd_off(D0, 1, 1));
;     const s16x4 l2 = tr_read(vb + v_rd_off(D0, 2, 0)), h2 = tr_read(vb + v_rd_off(D0, 2, 1)), l3 = tr_read(vb + v_rd_off(D0, 3, 0)), h3 = tr_read(vb + v_rd_off(D0, 3, 1));
;     ...
;     od = __builtin_amdgcn_mfma_f32_32x32x16_bf16(pa0, ATT_PK(l0, h0), od, 0, 0, 0);
;     od = __builtin_amdgcn_mfma_f32_32x32x16_bf16(pa1, ATT_PK(l1, h1), od, 0, 0, 0);
;     od = __builtin_amdgcn_mfma_f32_32x32x16_bf16(pa2, ATT_PK(l2, h2), od, 0, 0, 0);
;     od = __builtin_amdgcn_mfma_f32_32x32x16_bf16(pa3, ATT_PK(l3, h3), od, 0, 0, 0);
;     ...
; }
; __device__ __forceinline__ void pv_d0(f32x16* o, LAS const unsigned char* vb, bf16x8 pa0, bf16x8 pa1, bf16x8 pa2, bf16x8 pa3) {
.LBB0_633:
	ds_read_b128 v[76:79], v204 offset:49152
	ds_read_b128 v[80:83], v204 offset:57344
	ds_read_b128 v[192:195], v208 offset:49152
	ds_read_b128 v[232:235], v208 offset:57344
	v_add_f32_e32 v2, 0, v114
	v_add_f32_e32 v2, v1, v2
	s_waitcnt lgkmcnt(3)
	s_setprio 1
	v_mfma_f32_32x32x16_bf16 v[92:107], v[76:79], v[144:147], 0
	v_add_f32_e32 v2, v112, v2
	v_add_f32_e32 v2, v113, v2
	v_add_f32_e32 v2, v110, v2
	v_add_f32_e32 v2, v111, v2
	v_add_f32_e32 v2, v108, v2
	v_add_f32_e32 v2, v109, v2
	v_add_f32_e32 v2, v68, v2
	s_waitcnt lgkmcnt(2)
	v_mfma_f32_32x32x16_bf16 v[76:91], v[80:83], v[144:147], 0
	v_add_f32_e32 v2, v69, v2
	v_add_f32_e32 v2, v70, v2
	v_add_f32_e32 v2, v75, v2
	v_exp_f32_e32 v228, v164
	v_add_f32_e32 v2, v72, v2
	v_exp_f32_e32 v230, v165
	v_add_f32_e32 v2, v71, v2
	s_waitcnt lgkmcnt(1)
	v_mfma_f32_32x32x16_bf16 v[92:107], v[192:195], v[140:143], v[92:107]
	v_exp_f32_e32 v183, v166
	v_add_f32_e32 v2, v74, v2
	v_exp_f32_e32 v222, v167
	v_add_f32_e32 v2, v73, v2
	v_exp_f32_e32 v223, v168
	v_add_f32_e32 v2, v228, v2
	v_exp_f32_e32 v224, v169
	s_waitcnt lgkmcnt(0)
	v_mfma_f32_32x32x16_bf16 v[76:91], v[232:235], v[140:143], v[76:91]
	ds_read_b128 v[192:195], v209 offset:49152
	ds_read_b128 v[232:235], v209 offset:57344
	v_add_f32_e32 v2, v230, v2
	v_exp_f32_e32 v226, v170
	v_add_f32_e32 v2, v183, v2
	v_exp_f32_e32 v171, v171
	v_add_f32_e32 v2, v222, v2
	v_exp_f32_e32 v115, v172
	s_waitcnt lgkmcnt(1)
	v_mfma_f32_32x32x16_bf16 v[92:107], v[192:195], v[136:139], v[92:107]
	v_add_f32_e32 v2, v223, v2
	v_exp_f32_e32 v164, v173
	v_add_f32_e32 v2, v224, v2
	v_exp_f32_e32 v165, v174
	v_add_f32_e32 v2, v226, v2
	v_exp_f32_e32 v166, v175
	v_add_f32_e32 v2, v171, v2
	s_waitcnt lgkmcnt(0)
	v_mfma_f32_32x32x16_bf16 v[76:91], v[232:235], v[136:139], v[76:91]
	ds_read_b128 v[192:195], v210 offset:49152
	ds_read_b128 v[232:235], v210 offset:57344
	v_exp_f32_e32 v167, v176
	v_add_f32_e32 v2, v115, v2
	v_exp_f32_e32 v168, v177
	v_add_f32_e32 v2, v164, v2
	v_exp_f32_e32 v169, v178
	v_add_f32_e32 v2, v165, v2
	s_waitcnt lgkmcnt(1)
	v_mfma_f32_32x32x16_bf16 v[92:107], v[192:195], v[132:135], v[92:107]
	v_exp_f32_e32 v170, v179
	v_add_f32_e32 v2, v166, v2
	v_add_f32_e32 v2, v167, v2
	v_add_f32_e32 v2, v168, v2
	v_add_f32_e32 v2, v169, v2
	v_add_f32_e32 v2, v170, v2
	v_mov_b32_e32 v220, v2
	s_waitcnt lgkmcnt(0)
	v_mfma_f32_32x32x16_bf16 v[76:91], v[232:235], v[132:135], v[76:91]
	ds_read_b128 v[192:195], v202 offset:49152
	ds_read_b128 v[232:235], v202 offset:57344
	v_cvt_pk_bf16_f32 v68, v68, v69
	v_cvt_pk_bf16_f32 v69, v70, v75
	v_cvt_pk_bf16_f32 v70, v72, v71
	v_cvt_pk_bf16_f32 v71, v74, v73
	v_cvt_pk_bf16_f32 v72, v228, v230
	v_cvt_pk_bf16_f32 v73, v183, v222
	s_waitcnt lgkmcnt(1)
	v_mfma_f32_32x32x16_bf16 v[92:107], v[192:195], v[128:131], v[92:107]
	v_cvt_pk_bf16_f32 v74, v223, v224
	v_cvt_pk_bf16_f32 v75, v226, v171
	v_permlane32_swap_b32_e32 v2, v220
	v_cvt_pk_bf16_f32 v172, v114, v1
	v_cvt_pk_bf16_f32 v173, v112, v113
	v_cvt_pk_bf16_f32 v174, v110, v111
	s_waitcnt lgkmcnt(0)
	v_mfma_f32_32x32x16_bf16 v[76:91], v[232:235], v[128:131], v[76:91]
	ds_read_b128 v[192:195], v206 offset:49152
	ds_read_b128 v[232:235], v206 offset:57344
	v_cvt_pk_bf16_f32 v175, v108, v109
	v_permlane32_swap_b32_e32 v68, v70
	v_permlane32_swap_b32_e32 v69, v71
	v_permlane32_swap_b32_e32 v72, v74
	s_waitcnt lgkmcnt(1)
	v_mfma_f32_32x32x16_bf16 v[92:107], v[192:195], v[124:127], v[92:107]
	v_permlane32_swap_b32_e32 v73, v75
	v_cvt_pk_bf16_f32 v176, v115, v164
	v_cvt_pk_bf16_f32 v177, v165, v166
	v_cvt_pk_bf16_f32 v178, v167, v168
	v_cvt_pk_bf16_f32 v179, v169, v170
	v_permlane32_swap_b32_e32 v172, v174
	s_waitcnt lgkmcnt(0)
	v_mfma_f32_32x32x16_bf16 v[76:91], v[232:235], v[124:127], v[76:91]
	ds_read_b128 v[192:195], v212 offset:49152
	ds_read_b128 v[232:235], v212 offset:57344
	v_permlane32_swap_b32_e32 v173, v175
	v_permlane32_swap_b32_e32 v176, v178
	v_permlane32_swap_b32_e32 v177, v179
	s_waitcnt lgkmcnt(1)
	v_mfma_f32_32x32x16_bf16 v[92:107], v[192:195], v[120:123], v[92:107]
	s_waitcnt lgkmcnt(0)
	v_mfma_f32_32x32x16_bf16 v[76:91], v[232:235], v[120:123], v[76:91]
	ds_read_b128 v[192:195], v211 offset:49152
	ds_read_b128 v[232:235], v211 offset:57344
	s_waitcnt lgkmcnt(1)
	v_mfma_f32_32x32x16_bf16 v[92:107], v[192:195], v[116:119], v[92:107]
	s_waitcnt lgkmcnt(0)
	v_mfma_f32_32x32x16_bf16 v[76:91], v[232:235], v[116:119], v[76:91]
	s_setprio 0
	s_add_i32 s4, s84, 1
	s_add_i32 s5, s84, 33
	v_mad_u64_u32 v[108:109], s[0:1], s4, v242, v[190:191]
	v_mad_u64_u32 v[112:113], s[0:1], s5, v242, v[190:191]
	v_mad_u64_u32 v[164:165], s[0:1], s4, v242, v[188:189]
	v_mad_u64_u32 v[168:169], s[0:1], s5, v242, v[188:189]
	global_load_dwordx4 v[108:111], v[108:109], off
	s_nop 0
	global_load_dwordx4 v[112:115], v[112:113], off
	s_nop 0
	global_load_dwordx4 v[164:167], v[164:165], off offset:2048
	s_nop 0
	global_load_dwordx4 v[168:171], v[168:169], off offset:2048
	ds_read_b64_tr_b16 v[192:193], v196
	ds_read_b64_tr_b16 v[194:195], v196 offset:2048
	ds_read_b64_tr_b16 v[232:233], v196 offset:4096
	ds_read_b64_tr_b16 v[234:235], v196 offset:6144
	ds_read_b64_tr_b16 v[236:237], v196 offset:8192
	ds_read_b64_tr_b16 v[238:239], v196 offset:10240
	ds_read_b64_tr_b16 v[244:245], v196 offset:12288
	ds_read_b64_tr_b16 v[246:247], v196 offset:14336
	s_waitcnt lgkmcnt(6)
	s_setprio 1
	v_mfma_f32_32x32x16_bf16 v[52:67], v[172:175], v[192:195], v[52:67]
	v_add_u32_e32 v1, 64, v218
	s_sub_i32 s0, s84, 64
	s_cmp_le_i32 s0, s13
	s_mov_b32 s0, 2.0
	s_mov_b32 s1, 0x40400000
	s_waitcnt lgkmcnt(4)
	v_mfma_f32_32x32x16_bf16 v[52:67], v[68:71], v[232:235], v[52:67]
	s_waitcnt lgkmcnt(2)
; #define LAS __attribute__((address_space(3)))
; __device__ __forceinline__ s16x4 tr_read(LAS const unsigned char* p) { return __builtin_bit_cast(s16x4, __builtin_amdgcn_ds_read_tr16_b64_v4i16((LAS v4i16_t*)p)); }
; __device__ __forceinline__ void partialSM(f32x16& p0, f32x16& p1, float& m_reg, float& mn, float& alpha, int dq, float slopeL, bool diag, bool rowmasked) {
;     const float NEG = -__builtin_inff(); const float a0 = -slopeL * (float)dq;
; #pragma unroll
;     for (int r = 0; r < 16; ++r) { const int c = (r & 3) + 8 * (r >> 2);
;         p0[r] = fmaf(p0[r], CS, fmaf(slopeL, (float)c, a0)); p1[r] = fmaf(p1[r], CS, fmaf(slopeL, (float)(c + 32), a0)); }
;     if (diag) { asm volatile("" ::: "memory");
; #pragma unroll
;         for (int r = 0; r < 16; ++r) { const int c = (r & 3) + 8 * (r >> 2); if (c > dq) p0[r] = NEG; if (c + 32 > dq) p1[r] = NEG; } }
; template <int D0> __device__ __forceinline__ void pv_one(f32x16& od, LAS const unsigned char* vb, bf16x8 pa0, bf16x8 pa1, bf16x8 pa2, bf16x8 pa3) {
;     const s16x4 l0 = tr_read(vb + v_rd_off(D0, 0, 0)), h0 = tr_read(vb + v_rd_off(D0, 0, 1)), l1 = tr_read(vb + v_rd_off(D0, 1, 0)), h1 = tr_read(vb + v_rd_off(D0, 1, 1));
;     const s16x4 l2 = tr_read(vb + v_rd_off(D0, 2, 0)), h2 = tr_read(vb + v_rd_off(D0, 2, 1)), l3 = tr_read(vb + v_rd_off(D0, 3, 0)), h3 = tr_read(vb + v_rd_off(D0, 3, 1));
;     ...
;     od = __builtin_amdgcn_mfma_f32_32x32x16_bf16(pa0, ATT_PK(l0, h0), od, 0, 0, 0);
;     od = __builtin_amdgcn_mfma_f32_32x32x16_bf16(pa1, ATT_PK(l1, h1), od, 0, 0, 0);
;     od = __builtin_amdgcn_mfma_f32_32x32x16_bf16(pa2, ATT_PK(l2, h2), od, 0, 0, 0);
;     od = __builtin_amdgcn_mfma_f32_32x32x16_bf16(pa3, ATT_PK(l3, h3), od, 0, 0, 0);
;     ...
; }
; __device__ __forceinline__ void pv_d0(f32x16* o, LAS const unsigned char* vb, bf16x8 pa0, bf16x8 pa1, bf16x8 pa2, bf16x8 pa3) {
;     pv_one<0>(o[0], vb, pa0, pa1, pa2, pa3); pv_one<1>(o[1], vb, pa0, pa1, pa2, pa3); pv_one<2>(o[2], vb, pa0, pa1, pa2, pa3); pv_one<3>(o[3], vb, pa0, pa1, pa2, pa3);
; }
	v_mfma_f32_32x32x16_bf16 v[52:67], v[72:75], v[236:239], v[52:67]
	s_waitcnt lgkmcnt(0)
	v_mfma_f32_32x32x16_bf16 v[52:67], v[176:179], v[244:247], v[52:67]
	ds_read_b64_tr_b16 v[192:193], v196 offset:512
	ds_read_b64_tr_b16 v[194:195], v196 offset:2560
	ds_read_b64_tr_b16 v[232:233], v196 offset:4608
	ds_read_b64_tr_b16 v[234:235], v196 offset:6656
	ds_read_b64_tr_b16 v[236:237], v196 offset:8704
	ds_read_b64_tr_b16 v[238:239], v196 offset:10752
	ds_read_b64_tr_b16 v[244:245], v196 offset:12800
	ds_read_b64_tr_b16 v[246:247], v196 offset:14848
	s_waitcnt lgkmcnt(6)
	v_mfma_f32_32x32x16_bf16 v[36:51], v[172:175], v[192:195], v[36:51]
	s_waitcnt lgkmcnt(4)
	v_mfma_f32_32x32x16_bf16 v[36:51], v[68:71], v[232:235], v[36:51]
	s_waitcnt lgkmcnt(2)
	v_mfma_f32_32x32x16_bf16 v[36:51], v[72:75], v[236:239], v[36:51]
	s_waitcnt lgkmcnt(0)
	v_mfma_f32_32x32x16_bf16 v[36:51], v[176:179], v[244:247], v[36:51]
	ds_read_b64_tr_b16 v[192:193], v196 offset:1024
	ds_read_b64_tr_b16 v[194:195], v196 offset:3072
	ds_read_b64_tr_b16 v[232:233], v196 offset:5120
	ds_read_b64_tr_b16 v[234:235], v196 offset:7168
	ds_read_b64_tr_b16 v[236:237], v196 offset:9216
	ds_read_b64_tr_b16 v[238:239], v196 offset:11264
	ds_read_b64_tr_b16 v[244:245], v196 offset:13312
	ds_read_b64_tr_b16 v[246:247], v196 offset:15360
	s_waitcnt lgkmcnt(6)
	v_mfma_f32_32x32x16_bf16 v[20:35], v[172:175], v[192:195], v[20:35]
	s_waitcnt lgkmcnt(4)
	v_mfma_f32_32x32x16_bf16 v[20:35], v[68:71], v[232:235], v[20:35]
	s_waitcnt lgkmcnt(2)
	v_mfma_f32_32x32x16_bf16 v[20:35], v[72:75], v[236:239], v[20:35]
	s_waitcnt lgkmcnt(0)
	v_mfma_f32_32x32x16_bf16 v[20:35], v[176:179], v[244:247], v[20:35]
	ds_read_b64_tr_b16 v[192:193], v196 offset:1536
	ds_read_b64_tr_b16 v[194:195], v196 offset:3584
	ds_read_b64_tr_b16 v[232:233], v196 offset:5632
	ds_read_b64_tr_b16 v[234:235], v196 offset:7680
	ds_read_b64_tr_b16 v[236:237], v196 offset:9728
	ds_read_b64_tr_b16 v[238:239], v196 offset:11776
	ds_read_b64_tr_b16 v[244:245], v196 offset:13824
	ds_read_b64_tr_b16 v[246:247], v196 offset:15872
	s_waitcnt lgkmcnt(6)
	v_mfma_f32_32x32x16_bf16 v[4:19], v[172:175], v[192:195], v[4:19]
	s_waitcnt lgkmcnt(4)
	v_mfma_f32_32x32x16_bf16 v[4:19], v[68:71], v[232:235], v[4:19]
	v_cvt_f32_i32_e32 v68, v1
	v_mul_f32_e64 v172, -v182, v68
	v_fma_f32 v174, v186, s0, v172
	v_fma_f32 v175, v187, s1, v172
	s_mov_b32 s0, 0x41000000
	s_waitcnt lgkmcnt(2)
	v_mfma_f32_32x32x16_bf16 v[4:19], v[72:75], v[236:239], v[4:19]
	s_mov_b32 s1, 0x41100000
	v_fma_f32 v69, -v182, v68, v182
	v_mov_b32_e32 v68, v172
	v_fmac_f32_e32 v68, 0, v182
	v_fma_f32 v72, v186, s86, v172
	v_fma_f32 v73, v187, s87, v172
	v_pk_fma_f32 v[70:71], v[186:187], s[88:89], v[172:173] op_sel_hi:[1,1,0]
	v_pk_fma_f32 v[68:69], v[92:93], s[96:97], v[68:69] op_sel_hi:[1,0,1]
	s_waitcnt lgkmcnt(0)
	v_mfma_f32_32x32x16_bf16 v[4:19], v[176:179], v[244:247], v[4:19]
	s_setprio 0
	v_fma_f32 v176, v186, s0, v172
	v_fma_f32 v177, v187, s1, v172
	s_mov_b32 s0, 0x41200000
	s_mov_b32 s1, 0x41300000
	v_fma_f32 v178, v186, s0, v172
	v_fma_f32 v179, v187, s1, v172
	s_mov_b32 s0, 0x41800000
	s_mov_b32 s1, 0x41880000
	v_pk_fma_f32 v[192:193], v[186:187], s[0:1], v[172:173] op_sel_hi:[1,1,0]
	s_mov_b32 s0, 0x41900000
	s_mov_b32 s1, 0x41980000
	v_pk_fma_f32 v[74:75], v[186:187], s[0:1], v[172:173] op_sel_hi:[1,1,0]
	v_pk_fma_f32 v[70:71], v[106:107], s[96:97], v[70:71] op_sel_hi:[1,0,1]
	v_pk_fma_f32 v[72:73], v[104:105], s[96:97], v[72:73] op_sel_hi:[1,0,1]
	v_pk_fma_f32 v[74:75], v[102:103], s[96:97], v[74:75] op_sel_hi:[1,0,1]
	v_pk_fma_f32 v[92:93], v[100:101], s[96:97], v[192:193] op_sel_hi:[1,0,1]
	v_pk_fma_f32 v[98:99], v[98:99], s[96:97], v[178:179] op_sel_hi:[1,0,1]
	v_pk_fma_f32 v[96:97], v[96:97], s[96:97], v[176:177] op_sel_hi:[1,0,1]
	v_pk_fma_f32 v[94:95], v[94:95], s[96:97], v[174:175] op_sel_hi:[1,0,1]
	v_pk_fma_f32 v[100:101], v[186:187], s[90:91], v[172:173] op_sel_hi:[1,1,0]
	v_pk_fma_f32 v[102:103], v[186:187], s[92:93], v[172:173] op_sel_hi:[1,1,0]
	v_pk_fma_f32 v[104:105], v[186:187], s[94:95], v[172:173] op_sel_hi:[1,1,0]
	v_pk_fma_f32 v[106:107], v[186:187], s[68:69], v[172:173] op_sel_hi:[1,1,0]
	v_pk_fma_f32 v[174:175], v[186:187], s[70:71], v[172:173] op_sel_hi:[1,1,0]
	v_pk_fma_f32 v[176:177], v[186:187], s[72:73], v[172:173] op_sel_hi:[1,1,0]
	v_pk_fma_f32 v[178:179], v[186:187], s[74:75], v[172:173] op_sel_hi:[1,1,0]
	v_pk_fma_f32 v[172:173], v[184:185], s[76:77], v[172:173] op_sel_hi:[1,1,0]
	v_pk_fma_f32 v[90:91], v[90:91], s[96:97], v[178:179] op_sel_hi:[1,0,1]
	v_pk_fma_f32 v[88:89], v[88:89], s[96:97], v[176:177] op_sel_hi:[1,0,1]
	v_pk_fma_f32 v[86:87], v[86:87], s[96:97], v[174:175] op_sel_hi:[1,0,1]
	v_pk_fma_f32 v[84:85], v[84:85], s[96:97], v[106:107] op_sel_hi:[1,0,1]
	v_pk_fma_f32 v[82:83], v[82:83], s[96:97], v[104:105] op_sel_hi:[1,0,1]
	v_pk_fma_f32 v[80:81], v[80:81], s[96:97], v[102:103] op_sel_hi:[1,0,1]
	v_pk_fma_f32 v[78:79], v[78:79], s[96:97], v[100:101] op_sel_hi:[1,0,1]
	v_pk_fma_f32 v[76:77], v[76:77], s[96:97], v[172:173] op_sel_hi:[1,0,1]
	s_cbranch_scc1 .LBB0_637
; __device__ __forceinline__ void partialSM(f32x16& p0, f32x16& p1, float& m_reg, float& mn, float& alpha, int dq, float slopeL, bool diag, bool rowmasked) {
;     ...
;     for (int r = 0; r < 16; ++r) { const int c = (r & 3) + 8 * (r >> 2);
;         p0[r] = fmaf(p0[r], CS, fmaf(slopeL, (float)c, a0)); p1[r] = fmaf(p1[r], CS, fmaf(slopeL, (float)(c + 32), a0)); }
;     if (diag) { asm volatile("" ::: "memory");
; #pragma unroll
;         for (int r = 0; r < 16; ++r) { const int c = (r & 3) + 8 * (r >> 2); if (c > dq) p0[r] = NEG; if (c + 32 > dq) p1[r] = NEG; } }
	v_cmp_gt_i32_e64 s[64:65], 57, v1
	v_cmp_gt_i32_e64 s[66:67], 58, v1
	v_cmp_gt_i32_e64 s[62:63], 56, v1
	s_and_b64 s[64:65], s[66:67], s[64:65]
	v_cmp_gt_i32_e64 s[60:61], 51, v1
	s_and_b64 s[62:63], s[64:65], s[62:63]
	v_cmp_gt_i32_e64 s[58:59], 50, v1
	s_and_b64 s[60:61], s[62:63], s[60:61]
	v_cmp_gt_i32_e64 s[56:57], 49, v1
	s_and_b64 s[58:59], s[60:61], s[58:59]
	v_cmp_gt_i32_e64 s[54:55], 48, v1
	s_and_b64 s[56:57], s[58:59], s[56:57]
	v_cmp_gt_i32_e64 s[52:53], 43, v1
	s_and_b64 s[54:55], s[56:57], s[54:55]
	v_cmp_gt_i32_e64 s[50:51], 42, v1
	s_and_b64 s[52:53], s[54:55], s[52:53]
	v_cmp_gt_i32_e64 s[48:49], 41, v1
	s_and_b64 s[50:51], s[52:53], s[50:51]
	v_cmp_gt_i32_e64 s[46:47], 40, v1
	s_and_b64 s[48:49], s[50:51], s[48:49]
	v_cmp_gt_i32_e64 s[44:45], 35, v1
	s_and_b64 s[46:47], s[48:49], s[46:47]
	v_cmp_gt_i32_e64 s[42:43], 34, v1
	s_and_b64 s[44:45], s[46:47], s[44:45]
	v_cmp_gt_i32_e64 s[40:41], 33, v1
	s_and_b64 s[42:43], s[44:45], s[42:43]
	v_cmp_gt_i32_e64 s[38:39], 32, v1
	s_and_b64 s[40:41], s[42:43], s[40:41]
	s_and_b64 s[38:39], s[40:41], s[38:39]
	v_cmp_gt_i32_e32 vcc, 0, v1
	v_cmp_gt_i32_e64 s[0:1], 1, v1
	v_cmp_gt_i32_e64 s[8:9], 2, v1
	v_cmp_gt_i32_e64 s[10:11], 3, v1
	v_cmp_gt_i32_e64 s[14:15], 8, v1
	v_cmp_gt_i32_e64 s[16:17], 9, v1
	v_cmp_gt_i32_e64 s[18:19], 10, v1
	v_cmp_gt_i32_e64 s[20:21], 11, v1
	v_cmp_gt_i32_e64 s[22:23], 16, v1
	v_cmp_gt_i32_e64 s[24:25], 17, v1
	v_cmp_gt_i32_e64 s[26:27], 18, v1
	v_cmp_gt_i32_e64 s[28:29], 19, v1
	v_cmp_gt_i32_e64 s[30:31], 24, v1
	v_cmp_gt_i32_e64 s[34:35], 25, v1
	v_cmp_gt_i32_e64 s[36:37], 26, v1
	v_cndmask_b32_e64 v90, v90, v241, s[66:67]
	v_cndmask_b32_e64 v89, v89, v241, s[64:65]
	v_cndmask_b32_e64 v88, v88, v241, s[62:63]
	v_cndmask_b32_e64 v87, v87, v241, s[60:61]
	v_cndmask_b32_e64 v86, v86, v241, s[58:59]
	v_cndmask_b32_e64 v85, v85, v241, s[56:57]
	v_cndmask_b32_e64 v84, v84, v241, s[54:55]
	v_cndmask_b32_e64 v83, v83, v241, s[52:53]
	v_cndmask_b32_e64 v82, v82, v241, s[50:51]
	v_cndmask_b32_e64 v81, v81, v241, s[48:49]
	v_cndmask_b32_e64 v80, v80, v241, s[46:47]
	v_cndmask_b32_e64 v79, v79, v241, s[44:45]
	v_cndmask_b32_e64 v78, v78, v241, s[42:43]
	v_cndmask_b32_e64 v77, v77, v241, s[40:41]
	v_cndmask_b32_e64 v76, v76, v241, s[38:39]
	v_cmp_gt_i32_e64 s[38:39], 27, v1
	v_cmp_gt_i32_e64 s[40:41], 59, v1
	s_and_saveexec_b64 s[4:5], s[40:41]
	v_mov_b32_e32 v91, s85
	s_or_b64 exec, exec, s[4:5]
	s_and_b64 s[36:37], s[38:39], s[36:37]
	s_and_b64 s[34:35], s[36:37], s[34:35]
	s_and_b64 s[30:31], s[34:35], s[30:31]
	s_and_b64 s[28:29], s[30:31], s[28:29]
	s_and_b64 s[26:27], s[28:29], s[26:27]
	s_and_b64 s[24:25], s[26:27], s[24:25]
	s_and_b64 s[22:23], s[24:25], s[22:23]
	s_and_b64 s[20:21], s[22:23], s[20:21]
	s_and_b64 s[18:19], s[20:21], s[18:19]
	s_and_b64 s[16:17], s[18:19], s[16:17]
	s_and_b64 s[14:15], s[16:17], s[14:15]
	s_and_b64 s[10:11], s[14:15], s[10:11]
	s_and_b64 s[8:9], s[10:11], s[8:9]
	s_and_b64 s[0:1], s[8:9], s[0:1]
	s_and_b64 vcc, s[0:1], vcc
	v_cndmask_b32_e64 v70, v70, v241, s[36:37]
	v_cndmask_b32_e64 v73, v73, v241, s[34:35]
	v_cndmask_b32_e64 v72, v72, v241, s[30:31]
	v_cndmask_b32_e64 v75, v75, v241, s[28:29]
	v_cndmask_b32_e64 v74, v74, v241, s[26:27]
	v_cndmask_b32_e64 v93, v93, v241, s[24:25]
	v_cndmask_b32_e64 v92, v92, v241, s[22:23]
	v_cndmask_b32_e64 v99, v99, v241, s[20:21]
	v_cndmask_b32_e64 v98, v98, v241, s[18:19]
	v_cndmask_b32_e64 v97, v97, v241, s[16:17]
	v_cndmask_b32_e64 v96, v96, v241, s[14:15]
	v_cndmask_b32_e64 v95, v95, v241, s[10:11]
	v_cndmask_b32_e64 v94, v94, v241, s[8:9]
	v_cndmask_b32_e64 v69, v69, v241, s[0:1]
	v_cndmask_b32_e32 v68, v68, v241, vcc
	v_cndmask_b32_e64 v71, v71, v241, s[38:39]

; __device__ __forceinline__ void qkt(f32x16& p0, f32x16& p1, LAS const unsigned char* Ks, const bf16x8* qr, int r32, int hi) {
;     p0 = f32x16{}; p1 = f32x16{};
; #pragma unroll
;     for (int d0 = 0; d0 < 8; ++d0) { const int cb = (d0 * 16 + hi * 8) * 2;
;         const bf16x8 b0 = *(LAS const bf16x8*)(Ks + ATT_KSWZ(r32, cb));
;         const bf16x8 b1 = *(LAS const bf16x8*)(Ks + ATT_KSWZ(32 + r32, cb));
;         p0 = __builtin_amdgcn_mfma_f32_32x32x16_bf16(b0, qr[d0], p0, 0, 0, 0);
;         p1 = __builtin_amdgcn_mfma_f32_32x32x16_bf16(b1, qr[d0], p1, 0, 0, 0); }
; }
; __device__ __forceinline__ void partialSM(f32x16& p0, f32x16& p1, float& m_reg, float& mn, float& alpha, int dq, float slopeL, bool diag, bool rowmasked) {
;     const float NEG = -__builtin_inff(); const float a0 = -slopeL * (float)dq;
; #pragma unroll
;     for (int r = 0; r < 16; ++r) { const int c = (r & 3) + 8 * (r >> 2);
;         p0[r] = fmaf(p0[r], CS, fmaf(slopeL, (float)c, a0)); p1[r] = fmaf(p1[r], CS, fmaf(slopeL, (float)(c + 32), a0)); }
;     if (diag) { asm volatile("" ::: "memory");
; #pragma unroll
;         for (int r = 0; r < 16; ++r) { const int c = (r & 3) + 8 * (r >> 2); if (c > dq) p0[r] = NEG; if (c + 32 > dq) p1[r] = NEG; } }
;     if (rowmasked) {
; #pragma unroll
;         for (int r = 0; r < 16; ++r) { p0[r] = NEG; p1[r] = NEG; } }
;     float pmax = p0[0];
; #pragma unroll
;     for (int r = 1; r < 16; ++r) pmax = fmaxf(pmax, p0[r]);
; #pragma unroll
;     for (int r = 0; r < 16; ++r) pmax = fmaxf(pmax, p1[r]);
;     { auto rr = __builtin_amdgcn_permlane32_swap(__float_as_uint(pmax), __float_as_uint(pmax), false, false);
;       pmax = fmaxf(__uint_as_float(rr[0]), __uint_as_float(rr[1])); }
;     if (__builtin_expect(__all(pmax - m_reg <= THRL), 1)) { mn = m_reg; alpha = 1.f; }
;     else { mn = fmaxf(m_reg, pmax); alpha = __builtin_amdgcn_exp2f(m_reg - mn); m_reg = mn; }
; #pragma unroll
;     for (int r = 0; r < 16; ++r) { p0[r] = p0[r] - mn; p1[r] = p1[r] - mn; }
; #pragma unroll
;     for (int r = 0; r < 16; ++r) p0[r] = __builtin_amdgcn_exp2f(p0[r]);
; }
; __device__ __forceinline__ void finishSM(f32x16& p0, f32x16& p1, float alpha, float& l_reg, bf16x8& pa0, bf16x8& pa1, bf16x8& pa2, bf16x8& pa3) {
; #pragma unroll
;     for (int r = 0; r < 16; ++r) p1[r] = __builtin_amdgcn_exp2f(p1[r]);
;     float ps = 0;
; #pragma unroll
.LBB0_642:
	v_sub_f32_e32 v83, v106, v180
	v_sub_f32_e32 v84, v107, v180
	v_sub_f32_e32 v85, v94, v180
	v_sub_f32_e32 v86, v95, v180
	v_sub_f32_e32 v87, v96, v180
	v_sub_f32_e32 v88, v97, v180
	v_sub_f32_e32 v89, v98, v180
	v_sub_f32_e32 v90, v99, v180
	v_sub_f32_e32 v91, v92, v180
	v_sub_f32_e32 v92, v93, v180
	v_sub_f32_e32 v93, v104, v180
	v_sub_f32_e32 v94, v105, v180
	v_sub_f32_e32 v95, v102, v180
	v_sub_f32_e32 v96, v103, v180
	v_sub_f32_e32 v97, v100, v180
	v_sub_f32_e32 v98, v101, v180
	v_exp_f32_e32 v100, v83
	v_exp_f32_e32 v101, v84
	v_exp_f32_e32 v102, v85
	v_exp_f32_e32 v177, v86
	v_exp_f32_e32 v178, v87
	v_exp_f32_e32 v179, v88
	v_exp_f32_e32 v103, v89
	v_exp_f32_e32 v176, v90
	v_exp_f32_e32 v104, v91
	v_exp_f32_e32 v105, v92
	v_exp_f32_e32 v174, v93
	v_exp_f32_e32 v175, v94
	v_exp_f32_e32 v106, v95
	v_exp_f32_e32 v107, v96
	v_exp_f32_e32 v172, v97
	v_exp_f32_e32 v173, v98
	v_sub_f32_e32 v224, v78, v180
	v_sub_f32_e32 v226, v79, v180
	v_sub_f32_e32 v183, v76, v180
	v_sub_f32_e32 v222, v77, v180
	v_sub_f32_e32 v228, v80, v180
	v_sub_f32_e32 v230, v81, v180
	v_sub_f32_e32 v236, v75, v180
	v_sub_f32_e32 v237, v82, v180
	v_sub_f32_e32 v238, v73, v180
	v_sub_f32_e32 v239, v74, v180
	v_sub_f32_e32 v240, v71, v180
	v_sub_f32_e32 v244, v72, v180
	v_sub_f32_e32 v245, v69, v180
	v_sub_f32_e32 v246, v70, v180
	v_sub_f32_e32 v1, v1, v180
	v_sub_f32_e32 v247, v68, v180
	s_waitcnt lgkmcnt(0)
	s_barrier
	ds_read_b128 v[68:71], v204 offset:32768
	ds_read_b128 v[72:75], v204 offset:40960
	ds_read_b128 v[192:195], v208 offset:32768
	ds_read_b128 v[232:235], v208 offset:40960
	v_exp_f32_e32 v183, v183
	v_exp_f32_e32 v1, v1
	s_waitcnt lgkmcnt(3)
	s_setprio 1
	v_mfma_f32_32x32x16_bf16 v[84:99], v[68:71], v[144:147], 0
	s_waitcnt lgkmcnt(2)
	v_mfma_f32_32x32x16_bf16 v[68:83], v[72:75], v[144:147], 0
	s_waitcnt lgkmcnt(1)
	v_mfma_f32_32x32x16_bf16 v[84:99], v[192:195], v[140:143], v[84:99]
	s_waitcnt lgkmcnt(0)
	v_mfma_f32_32x32x16_bf16 v[68:83], v[232:235], v[140:143], v[68:83]
	ds_read_b128 v[192:195], v209 offset:32768
	ds_read_b128 v[232:235], v209 offset:40960
	s_waitcnt lgkmcnt(1)
	v_mfma_f32_32x32x16_bf16 v[84:99], v[192:195], v[136:139], v[84:99]
	s_waitcnt lgkmcnt(0)
	v_mfma_f32_32x32x16_bf16 v[68:83], v[232:235], v[136:139], v[68:83]
	ds_read_b128 v[192:195], v210 offset:32768
	ds_read_b128 v[232:235], v210 offset:40960
	s_waitcnt lgkmcnt(1)
	v_mfma_f32_32x32x16_bf16 v[84:99], v[192:195], v[132:135], v[84:99]
	s_waitcnt lgkmcnt(0)
	v_mfma_f32_32x32x16_bf16 v[68:83], v[232:235], v[132:135], v[68:83]
	ds_read_b128 v[192:195], v202 offset:32768
	ds_read_b128 v[232:235], v202 offset:40960
	s_waitcnt lgkmcnt(1)
	v_mfma_f32_32x32x16_bf16 v[84:99], v[192:195], v[128:131], v[84:99]
	s_waitcnt lgkmcnt(0)
	v_mfma_f32_32x32x16_bf16 v[68:83], v[232:235], v[128:131], v[68:83]
	ds_read_b128 v[192:195], v206 offset:32768
	ds_read_b128 v[232:235], v206 offset:40960
	s_waitcnt lgkmcnt(1)
	v_mfma_f32_32x32x16_bf16 v[84:99], v[192:195], v[124:127], v[84:99]
	s_waitcnt lgkmcnt(0)
	v_mfma_f32_32x32x16_bf16 v[68:83], v[232:235], v[124:127], v[68:83]
	ds_read_b128 v[192:195], v212 offset:32768
	ds_read_b128 v[232:235], v212 offset:40960
	s_waitcnt lgkmcnt(1)
	v_mfma_f32_32x32x16_bf16 v[84:99], v[192:195], v[120:123], v[84:99]
	s_waitcnt lgkmcnt(0)
	v_mfma_f32_32x32x16_bf16 v[68:83], v[232:235], v[120:123], v[68:83]
	ds_read_b128 v[192:195], v211 offset:32768
	ds_read_b128 v[232:235], v211 offset:40960
	s_waitcnt lgkmcnt(1)
	v_mfma_f32_32x32x16_bf16 v[84:99], v[192:195], v[116:119], v[84:99]
	s_setprio 0
	v_exp_f32_e32 v193, v224
	v_add_f32_e32 v224, 0, v100
	v_add_f32_e32 v224, v101, v224
	v_add_f32_e32 v224, v102, v224
	v_add_f32_e32 v224, v177, v224
	v_add_f32_e32 v224, v178, v224
	v_add_f32_e32 v224, v179, v224
	v_add_f32_e32 v224, v103, v224
	v_add_f32_e32 v224, v176, v224
	v_add_f32_e32 v224, v104, v224
	v_add_f32_e32 v224, v105, v224
	v_add_f32_e32 v224, v174, v224
	v_add_f32_e32 v224, v175, v224
	v_add_f32_e32 v224, v106, v224
	v_exp_f32_e32 v192, v222
	v_add_f32_e32 v224, v107, v224
	v_add_f32_e32 v224, v172, v224
	v_exp_f32_e32 v194, v226
	v_add_f32_e32 v224, v173, v224
	v_exp_f32_e32 v195, v228
	v_add_f32_e32 v224, v183, v224
	v_exp_f32_e32 v222, v230
	v_add_f32_e32 v224, v192, v224
	v_exp_f32_e32 v228, v236
	v_add_f32_e32 v224, v193, v224
	v_exp_f32_e32 v230, v237
	v_add_f32_e32 v224, v194, v224
	s_waitcnt lgkmcnt(0)
	s_setprio 1
	v_mfma_f32_32x32x16_bf16 v[68:83], v[232:235], v[116:119], v[68:83]
	s_setprio 0
	v_exp_f32_e32 v232, v238
	v_add_f32_e32 v224, v195, v224
	v_exp_f32_e32 v233, v239
	v_add_f32_e32 v224, v222, v224
	v_exp_f32_e32 v234, v240
	v_add_f32_e32 v224, v228, v224
	v_exp_f32_e32 v235, v244
	v_add_f32_e32 v224, v230, v224
	v_exp_f32_e32 v236, v245
	v_add_f32_e32 v224, v232, v224
	v_exp_f32_e32 v237, v246
	v_add_f32_e32 v224, v233, v224
	v_add_f32_e32 v224, v234, v224
	v_exp_f32_e32 v238, v247
	v_add_f32_e32 v224, v235, v224
	v_add_f32_e32 v224, v236, v224
	v_add_f32_e32 v224, v237, v224
	v_add_f32_e32 v224, v1, v224
	v_add_f32_e32 v224, v238, v224
	v_mov_b32_e32 v226, v224
	v_cvt_pk_bf16_f32 v100, v100, v101
	v_cvt_pk_bf16_f32 v101, v102, v177
	v_cvt_pk_bf16_f32 v102, v178, v179
	v_cvt_pk_bf16_f32 v103, v103, v176
	v_cvt_pk_bf16_f32 v104, v104, v105
	v_cvt_pk_bf16_f32 v105, v174, v175
	v_cvt_pk_bf16_f32 v106, v106, v107
	v_cvt_pk_bf16_f32 v107, v172, v173
	v_cvt_pk_bf16_f32 v172, v183, v192
	v_cvt_pk_bf16_f32 v173, v193, v194
	v_cvt_pk_bf16_f32 v174, v195, v222
	v_cvt_pk_bf16_f32 v175, v228, v230
	v_cvt_pk_bf16_f32 v176, v232, v233
	v_cvt_pk_bf16_f32 v177, v234, v235
	v_cvt_pk_bf16_f32 v178, v236, v237
	v_cvt_pk_bf16_f32 v179, v1, v238
	v_permlane32_swap_b32_e32 v224, v226
	v_permlane32_swap_b32_e32 v100, v102
	v_permlane32_swap_b32_e32 v101, v103
	v_permlane32_swap_b32_e32 v104, v106
	v_permlane32_swap_b32_e32 v105, v107
	v_permlane32_swap_b32_e32 v172, v174
	v_permlane32_swap_b32_e32 v173, v175
	v_permlane32_swap_b32_e32 v176, v178
	v_permlane32_swap_b32_e32 v177, v179
	s_cmp_ge_i32 s85, s83
	s_cbranch_scc1 .LBB0_644
	s_add_i32 s4, s84, 0x41
	s_add_i32 s5, s84, 0x61
	v_mad_u64_u32 v[148:149], s[0:1], s4, v242, v[190:191]
	v_mad_u64_u32 v[152:153], s[0:1], s5, v242, v[190:191]
	v_mad_u64_u32 v[156:157], s[0:1], s4, v242, v[188:189]
	v_mad_u64_u32 v[160:161], s[0:1], s5, v242, v[188:189]
	global_load_dwordx4 v[148:151], v[148:149], off
	s_nop 0
	global_load_dwordx4 v[152:155], v[152:153], off
	s_nop 0
	global_load_dwordx4 v[156:159], v[156:157], off offset:2048
	s_nop 0
	global_load_dwordx4 v[160:163], v[160:161], off offset:2048
; #define LAS __attribute__((address_space(3)))
; __device__ __forceinline__ s16x4 tr_read(LAS const unsigned char* p) { return __builtin_bit_cast(s16x4, __builtin_amdgcn_ds_read_tr16_b64_v4i16((LAS v4i16_t*)p)); }
; __device__ __forceinline__ void partialSM(f32x16& p0, f32x16& p1, float& m_reg, float& mn, float& alpha, int dq, float slopeL, bool diag, bool rowmasked) {
;     const float NEG = -__builtin_inff(); const float a0 = -slopeL * (float)dq;
; #pragma unroll
;     for (int r = 0; r < 16; ++r) { const int c = (r & 3) + 8 * (r >> 2);
;         p0[r] = fmaf(p0[r], CS, fmaf(slopeL, (float)c, a0)); p1[r] = fmaf(p1[r], CS, fmaf(slopeL, (float)(c + 32), a0)); }
; template <int D0> __device__ __forceinline__ void pv_one(f32x16& od, LAS const unsigned char* vb, bf16x8 pa0, bf16x8 pa1, bf16x8 pa2, bf16x8 pa3) {
;     const s16x4 l0 = tr_read(vb + v_rd_off(D0, 0, 0)), h0 = tr_read(vb + v_rd_off(D0, 0, 1)), l1 = tr_read(vb + v_rd_off(D0, 1, 0)), h1 = tr_read(vb + v_rd_off(D0, 1, 1));
;     const s16x4 l2 = tr_read(vb + v_rd_off(D0, 2, 0)), h2 = tr_read(vb + v_rd_off(D0, 2, 1)), l3 = tr_read(vb + v_rd_off(D0, 3, 0)), h3 = tr_read(vb + v_rd_off(D0, 3, 1));
;     ...
;     od = __builtin_amdgcn_mfma_f32_32x32x16_bf16(pa0, ATT_PK(l0, h0), od, 0, 0, 0);
;     od = __builtin_amdgcn_mfma_f32_32x32x16_bf16(pa1, ATT_PK(l1, h1), od, 0, 0, 0);
;     od = __builtin_amdgcn_mfma_f32_32x32x16_bf16(pa2, ATT_PK(l2, h2), od, 0, 0, 0);
;     od = __builtin_amdgcn_mfma_f32_32x32x16_bf16(pa3, ATT_PK(l3, h3), od, 0, 0, 0);
;     ...
; }
; __device__ __forceinline__ void pv_d0(f32x16* o, LAS const unsigned char* vb, bf16x8 pa0, bf16x8 pa1, bf16x8 pa2, bf16x8 pa3) {
;     pv_one<0>(o[0], vb, pa0, pa1, pa2, pa3); pv_one<1>(o[1], vb, pa0, pa1, pa2, pa3); pv_one<2>(o[2], vb, pa0, pa1, pa2, pa3); pv_one<3>(o[3], vb, pa0, pa1, pa2, pa3);
; }
.LBB0_644:
	ds_read_b64_tr_b16 v[192:193], v196 offset:16384
	ds_read_b64_tr_b16 v[194:195], v196 offset:18432
	ds_read_b64_tr_b16 v[232:233], v196 offset:20480
	ds_read_b64_tr_b16 v[234:235], v196 offset:22528
	ds_read_b64_tr_b16 v[236:237], v196 offset:24576
	ds_read_b64_tr_b16 v[238:239], v196 offset:26624
	ds_read_b64_tr_b16 v[244:245], v196 offset:28672
	ds_read_b64_tr_b16 v[246:247], v196 offset:30720
	s_waitcnt lgkmcnt(6)
	s_setprio 1
	v_mfma_f32_32x32x16_bf16 v[52:67], v[100:103], v[192:195], v[52:67]
	v_cvt_f32_i32_e32 v1, v218
	s_mov_b32 s0, 2.0
	s_mov_b32 s1, 0x40400000
	v_mov_b32_e32 v183, v182
	s_cmp_le_i32 s84, s13
	s_waitcnt lgkmcnt(4)
	v_mfma_f32_32x32x16_bf16 v[52:67], v[104:107], v[232:235], v[52:67]
	s_waitcnt lgkmcnt(2)
	v_mfma_f32_32x32x16_bf16 v[52:67], v[172:175], v[236:239], v[52:67]
	s_waitcnt lgkmcnt(0)
	v_mfma_f32_32x32x16_bf16 v[52:67], v[176:179], v[244:247], v[52:67]
	ds_read_b64_tr_b16 v[192:193], v196 offset:16896
	ds_read_b64_tr_b16 v[194:195], v196 offset:18944
	ds_read_b64_tr_b16 v[232:233], v196 offset:20992
	ds_read_b64_tr_b16 v[234:235], v196 offset:23040
	ds_read_b64_tr_b16 v[236:237], v196 offset:25088
	ds_read_b64_tr_b16 v[238:239], v196 offset:27136
	ds_read_b64_tr_b16 v[244:245], v196 offset:29184
	ds_read_b64_tr_b16 v[246:247], v196 offset:31232
	s_waitcnt lgkmcnt(6)
	v_mfma_f32_32x32x16_bf16 v[36:51], v[100:103], v[192:195], v[36:51]
	s_waitcnt lgkmcnt(4)
	v_mfma_f32_32x32x16_bf16 v[36:51], v[104:107], v[232:235], v[36:51]
	s_waitcnt lgkmcnt(2)
	v_mfma_f32_32x32x16_bf16 v[36:51], v[172:175], v[236:239], v[36:51]
	s_waitcnt lgkmcnt(0)
	v_mfma_f32_32x32x16_bf16 v[36:51], v[176:179], v[244:247], v[36:51]
	ds_read_b64_tr_b16 v[192:193], v196 offset:17408
	ds_read_b64_tr_b16 v[194:195], v196 offset:19456
	ds_read_b64_tr_b16 v[232:233], v196 offset:21504
	ds_read_b64_tr_b16 v[234:235], v196 offset:23552
	ds_read_b64_tr_b16 v[236:237], v196 offset:25600
	ds_read_b64_tr_b16 v[238:239], v196 offset:27648
	ds_read_b64_tr_b16 v[244:245], v196 offset:29696
	ds_read_b64_tr_b16 v[246:247], v196 offset:31744
	s_waitcnt lgkmcnt(6)
	v_mfma_f32_32x32x16_bf16 v[20:35], v[100:103], v[192:195], v[20:35]
	s_waitcnt lgkmcnt(4)
	v_mfma_f32_32x32x16_bf16 v[20:35], v[104:107], v[232:235], v[20:35]
	s_waitcnt lgkmcnt(2)
	v_mfma_f32_32x32x16_bf16 v[20:35], v[172:175], v[236:239], v[20:35]
	s_waitcnt lgkmcnt(0)
	v_mfma_f32_32x32x16_bf16 v[20:35], v[176:179], v[244:247], v[20:35]
	ds_read_b64_tr_b16 v[192:193], v196 offset:17920
	ds_read_b64_tr_b16 v[194:195], v196 offset:19968
	ds_read_b64_tr_b16 v[232:233], v196 offset:22016
	ds_read_b64_tr_b16 v[234:235], v196 offset:24064
	ds_read_b64_tr_b16 v[236:237], v196 offset:26112
	ds_read_b64_tr_b16 v[238:239], v196 offset:28160
	ds_read_b64_tr_b16 v[244:245], v196 offset:30208
	ds_read_b64_tr_b16 v[246:247], v196 offset:32256
	s_waitcnt lgkmcnt(6)
	v_mfma_f32_32x32x16_bf16 v[4:19], v[100:103], v[192:195], v[4:19]
	v_mul_f32_e64 v100, -v182, v1
	v_mov_b32_e32 v102, v100
	v_fma_f32 v103, -v182, v1, v182
	v_fmac_f32_e32 v102, 0, v182
	v_fma_f32 v192, v186, s88, v100
	v_fma_f32 v193, v187, s89, v100
	v_pk_fma_f32 v[84:85], v[84:85], s[96:97], v[102:103] op_sel_hi:[1,0,1]
	v_pk_fma_f32 v[98:99], v[98:99], s[96:97], v[192:193] op_sel_hi:[1,0,1]
	s_waitcnt lgkmcnt(4)
	v_mfma_f32_32x32x16_bf16 v[4:19], v[104:107], v[232:235], v[4:19]
	v_fma_f32 v104, v186, s0, v100
	v_fma_f32 v105, v187, s1, v100
	s_mov_b32 s0, 0x41000000
	s_mov_b32 s1, 0x41100000
	v_fma_f32 v106, v186, s0, v100
	v_fma_f32 v107, v187, s1, v100
	s_mov_b32 s0, 0x41200000
	s_mov_b32 s1, 0x41300000
	v_pk_fma_f32 v[88:89], v[88:89], s[96:97], v[106:107] op_sel_hi:[1,0,1]
	s_waitcnt lgkmcnt(2)
	v_mfma_f32_32x32x16_bf16 v[4:19], v[172:175], v[236:239], v[4:19]
	v_fma_f32 v172, v186, s0, v100
	v_fma_f32 v173, v187, s1, v100
	s_mov_b32 s0, 0x41800000
	s_mov_b32 s1, 0x41880000
	v_fma_f32 v174, v186, s0, v100
	v_fma_f32 v175, v187, s1, v100
	s_mov_b32 s0, 0x41900000
	s_mov_b32 s1, 0x41980000
	v_pk_fma_f32 v[92:93], v[92:93], s[96:97], v[174:175] op_sel_hi:[1,0,1]
	s_waitcnt lgkmcnt(0)
	v_mfma_f32_32x32x16_bf16 v[4:19], v[176:179], v[244:247], v[4:19]
	s_setprio 0
	v_fma_f32 v176, v186, s0, v100
	v_fma_f32 v177, v187, s1, v100
	v_fma_f32 v178, v186, s86, v100
	v_fma_f32 v179, v187, s87, v100
	v_fma_f32 v94, v94, s96, v176
	v_fma_f32 v95, v95, s96, v177
	v_pk_fma_f32 v[96:97], v[96:97], s[96:97], v[178:179] op_sel_hi:[1,0,1]
	v_pk_fma_f32 v[90:91], v[90:91], s[96:97], v[172:173] op_sel_hi:[1,0,1]
	v_pk_fma_f32 v[86:87], v[86:87], s[96:97], v[104:105] op_sel_hi:[1,0,1]
	v_pk_fma_f32 v[104:105], v[182:183], s[90:91], v[100:101] op_sel_hi:[1,1,0]
	v_pk_fma_f32 v[106:107], v[182:183], s[92:93], v[100:101] op_sel_hi:[1,1,0]
	v_pk_fma_f32 v[172:173], v[182:183], s[94:95], v[100:101] op_sel_hi:[1,1,0]
	v_pk_fma_f32 v[102:103], v[182:183], s[68:69], v[100:101] op_sel_hi:[1,1,0]
	v_pk_fma_f32 v[174:175], v[182:183], s[70:71], v[100:101] op_sel_hi:[1,1,0]
	v_pk_fma_f32 v[176:177], v[182:183], s[72:73], v[100:101] op_sel_hi:[1,1,0]
	v_pk_fma_f32 v[178:179], v[182:183], s[74:75], v[100:101] op_sel_hi:[1,1,0]
	v_pk_fma_f32 v[192:193], v[184:185], s[76:77], v[100:101] op_sel_hi:[1,1,0]
	v_pk_fma_f32 v[82:83], v[82:83], s[96:97], v[178:179] op_sel_hi:[1,0,1]
	v_pk_fma_f32 v[80:81], v[80:81], s[96:97], v[176:177] op_sel_hi:[1,0,1]
	v_pk_fma_f32 v[100:101], v[78:79], s[96:97], v[174:175] op_sel_hi:[1,0,1]
	v_pk_fma_f32 v[102:103], v[76:77], s[96:97], v[102:103] op_sel_hi:[1,0,1]
	v_pk_fma_f32 v[74:75], v[74:75], s[96:97], v[172:173] op_sel_hi:[1,0,1]
	v_pk_fma_f32 v[72:73], v[72:73], s[96:97], v[106:107] op_sel_hi:[1,0,1]
	v_pk_fma_f32 v[70:71], v[70:71], s[96:97], v[104:105] op_sel_hi:[1,0,1]
	v_pk_fma_f32 v[68:69], v[68:69], s[96:97], v[192:193] op_sel_hi:[1,0,1]
	s_cbranch_scc1 .LBB0_648
; __device__ __forceinline__ void partialSM(f32x16& p0, f32x16& p1, float& m_reg, float& mn, float& alpha, int dq, float slopeL, bool diag, bool rowmasked) {
;     ...
;     for (int r = 0; r < 16; ++r) { const int c = (r & 3) + 8 * (r >> 2);
;         p0[r] = fmaf(p0[r], CS, fmaf(slopeL, (float)c, a0)); p1[r] = fmaf(p1[r], CS, fmaf(slopeL, (float)(c + 32), a0)); }
;     if (diag) { asm volatile("" ::: "memory");
; #pragma unroll
;         for (int r = 0; r < 16; ++r) { const int c = (r & 3) + 8 * (r >> 2); if (c > dq) p0[r] = NEG; if (c + 32 > dq) p1[r] = NEG; } }
	v_cmp_gt_i32_e64 s[64:65], 57, v218
	v_cmp_gt_i32_e64 s[66:67], 58, v218
	v_cmp_gt_i32_e64 s[62:63], 56, v218
	s_and_b64 s[64:65], s[66:67], s[64:65]
	v_cmp_gt_i32_e64 s[60:61], 51, v218
	s_and_b64 s[62:63], s[64:65], s[62:63]
	v_cmp_gt_i32_e64 s[58:59], 50, v218
	s_and_b64 s[60:61], s[62:63], s[60:61]
	v_cmp_gt_i32_e64 s[56:57], 49, v218
	s_and_b64 s[58:59], s[60:61], s[58:59]
	v_cmp_gt_i32_e64 s[54:55], 48, v218
	s_and_b64 s[56:57], s[58:59], s[56:57]
	v_cmp_gt_i32_e64 s[52:53], 43, v218
	s_and_b64 s[54:55], s[56:57], s[54:55]
	v_cmp_gt_i32_e64 s[50:51], 42, v218
	s_and_b64 s[52:53], s[54:55], s[52:53]
	v_cmp_gt_i32_e64 s[48:49], 41, v218
	s_and_b64 s[50:51], s[52:53], s[50:51]
	v_cmp_gt_i32_e64 s[46:47], 40, v218
	s_and_b64 s[48:49], s[50:51], s[48:49]
	v_cmp_gt_i32_e64 s[44:45], 35, v218
	s_and_b64 s[46:47], s[48:49], s[46:47]
	v_cmp_gt_i32_e64 s[42:43], 34, v218
	s_and_b64 s[44:45], s[46:47], s[44:45]
	v_cmp_gt_i32_e64 s[40:41], 33, v218
	s_and_b64 s[42:43], s[44:45], s[42:43]
	v_cmp_gt_i32_e64 s[38:39], 32, v218
	s_and_b64 s[40:41], s[42:43], s[40:41]
	s_and_b64 s[38:39], s[40:41], s[38:39]
	v_cmp_gt_i32_e32 vcc, 0, v218
	v_cmp_gt_i32_e64 s[0:1], 1, v218
	v_cmp_gt_i32_e64 s[8:9], 2, v218
	v_cmp_gt_i32_e64 s[10:11], 3, v218
	v_cmp_gt_i32_e64 s[14:15], 8, v218
	v_cmp_gt_i32_e64 s[16:17], 9, v218
	v_cmp_gt_i32_e64 s[18:19], 10, v218
	v_cmp_gt_i32_e64 s[20:21], 11, v218
	v_cmp_gt_i32_e64 s[22:23], 16, v218
	v_cmp_gt_i32_e64 s[24:25], 17, v218
	v_cmp_gt_i32_e64 s[26:27], 18, v218
	v_cmp_gt_i32_e64 s[28:29], 19, v218
	v_cmp_gt_i32_e64 s[30:31], 24, v218
	v_cmp_gt_i32_e64 s[34:35], 25, v218
	v_cmp_gt_i32_e64 s[36:37], 26, v218
	v_cndmask_b32_e64 v82, v82, v241, s[66:67]
	v_cndmask_b32_e64 v81, v81, v241, s[64:65]
	v_cndmask_b32_e64 v80, v80, v241, s[62:63]
	v_cndmask_b32_e64 v101, v101, v241, s[60:61]
	v_cndmask_b32_e64 v100, v100, v241, s[58:59]
	v_cndmask_b32_e64 v103, v103, v241, s[56:57]
	v_cndmask_b32_e64 v102, v102, v241, s[54:55]
	v_cndmask_b32_e64 v75, v75, v241, s[52:53]
	v_cndmask_b32_e64 v74, v74, v241, s[50:51]
	v_cndmask_b32_e64 v73, v73, v241, s[48:49]
	v_cndmask_b32_e64 v72, v72, v241, s[46:47]
	v_cndmask_b32_e64 v71, v71, v241, s[44:45]
	v_cndmask_b32_e64 v70, v70, v241, s[42:43]
	v_cndmask_b32_e64 v69, v69, v241, s[40:41]
	v_cndmask_b32_e64 v68, v68, v241, s[38:39]
	v_cmp_gt_i32_e64 s[38:39], 27, v218
	v_cmp_gt_i32_e64 s[40:41], 59, v218
	s_and_saveexec_b64 s[4:5], s[40:41]
	v_mov_b32_e32 v83, s12
	s_or_b64 exec, exec, s[4:5]
	s_and_b64 s[36:37], s[38:39], s[36:37]
	s_and_b64 s[34:35], s[36:37], s[34:35]
	s_and_b64 s[30:31], s[34:35], s[30:31]
	s_and_b64 s[28:29], s[30:31], s[28:29]
	s_and_b64 s[26:27], s[28:29], s[26:27]
	s_and_b64 s[24:25], s[26:27], s[24:25]
	s_and_b64 s[22:23], s[24:25], s[22:23]
	s_and_b64 s[20:21], s[22:23], s[20:21]
	s_and_b64 s[18:19], s[20:21], s[18:19]
	s_and_b64 s[16:17], s[18:19], s[16:17]
	s_and_b64 s[14:15], s[16:17], s[14:15]
	s_and_b64 s[10:11], s[14:15], s[10:11]
	s_and_b64 s[8:9], s[10:11], s[8:9]
	s_and_b64 s[0:1], s[8:9], s[0:1]
	s_and_b64 vcc, s[0:1], vcc
	v_cndmask_b32_e64 v98, v98, v241, s[36:37]
	v_cndmask_b32_e64 v97, v97, v241, s[34:35]
	v_cndmask_b32_e64 v96, v96, v241, s[30:31]
	v_cndmask_b32_e64 v95, v95, v241, s[28:29]
	v_cndmask_b32_e64 v94, v94, v241, s[26:27]
	v_cndmask_b32_e64 v93, v93, v241, s[24:25]
	v_cndmask_b32_e64 v92, v92, v241, s[22:23]
	v_cndmask_b32_e64 v91, v91, v241, s[20:21]
	v_cndmask_b32_e64 v90, v90, v241, s[18:19]
	v_cndmask_b32_e64 v89, v89, v241, s[16:17]
	v_cndmask_b32_e64 v88, v88, v241, s[14:15]
	v_cndmask_b32_e64 v87, v87, v241, s[10:11]
	v_cndmask_b32_e64 v86, v86, v241, s[8:9]
	v_cndmask_b32_e64 v85, v85, v241, s[0:1]
	v_cndmask_b32_e32 v84, v84, v241, vcc
	v_cndmask_b32_e64 v99, v99, v241, s[38:39]

; __device__ __forceinline__ void qkt(f32x16& p0, f32x16& p1, LAS const unsigned char* Ks, const bf16x8* qr, int r32, int hi) {
;     p0 = f32x16{}; p1 = f32x16{};
; #pragma unroll
;     for (int d0 = 0; d0 < 8; ++d0) { const int cb = (d0 * 16 + hi * 8) * 2;
;         const bf16x8 b0 = *(LAS const bf16x8*)(Ks + ATT_KSWZ(r32, cb));
;         const bf16x8 b1 = *(LAS const bf16x8*)(Ks + ATT_KSWZ(32 + r32, cb));
;         p0 = __builtin_amdgcn_mfma_f32_32x32x16_bf16(b0, qr[d0], p0, 0, 0, 0);
;         p1 = __builtin_amdgcn_mfma_f32_32x32x16_bf16(b1, qr[d0], p1, 0, 0, 0); }
; }
; __device__ __forceinline__ void partialSM(f32x16& p0, f32x16& p1, float& m_reg, float& mn, float& alpha, int dq, float slopeL, bool diag, bool rowmasked) {
;     const float NEG = -__builtin_inff(); const float a0 = -slopeL * (float)dq;
; #pragma unroll
;     for (int r = 0; r < 16; ++r) { const int c = (r & 3) + 8 * (r >> 2);
;         p0[r] = fmaf(p0[r], CS, fmaf(slopeL, (float)c, a0)); p1[r] = fmaf(p1[r], CS, fmaf(slopeL, (float)(c + 32), a0)); }
;     if (diag) { asm volatile("" ::: "memory");
; #pragma unroll
;         for (int r = 0; r < 16; ++r) { const int c = (r & 3) + 8 * (r >> 2); if (c > dq) p0[r] = NEG; if (c + 32 > dq) p1[r] = NEG; } }
;     if (rowmasked) {
; #pragma unroll
;         for (int r = 0; r < 16; ++r) { p0[r] = NEG; p1[r] = NEG; } }
;     float pmax = p0[0];
; #pragma unroll
;     for (int r = 1; r < 16; ++r) pmax = fmaxf(pmax, p0[r]);
; #pragma unroll
;     for (int r = 0; r < 16; ++r) pmax = fmaxf(pmax, p1[r]);
;     { auto rr = __builtin_amdgcn_permlane32_swap(__float_as_uint(pmax), __float_as_uint(pmax), false, false);
;       pmax = fmaxf(__uint_as_float(rr[0]), __uint_as_float(rr[1])); }
;     if (__builtin_expect(__all(pmax - m_reg <= THRL), 1)) { mn = m_reg; alpha = 1.f; }
;     else { mn = fmaxf(m_reg, pmax); alpha = __builtin_amdgcn_exp2f(m_reg - mn); m_reg = mn; }
; #pragma unroll
;     for (int r = 0; r < 16; ++r) { p0[r] = p0[r] - mn; p1[r] = p1[r] - mn; }
; #pragma unroll
;     for (int r = 0; r < 16; ++r) p0[r] = __builtin_amdgcn_exp2f(p0[r]);
; }
; __device__ __forceinline__ void finishSM(f32x16& p0, f32x16& p1, float alpha, float& l_reg, bf16x8& pa0, bf16x8& pa1, bf16x8& pa2, bf16x8& pa3) {
; #pragma unroll
;     for (int r = 0; r < 16; ++r) p1[r] = __builtin_amdgcn_exp2f(p1[r]);
;     float ps = 0;
; #pragma unroll
.LBB0_820:
	ds_read_b128 v[82:85], v206 offset:49152
	ds_read_b128 v[86:89], v206 offset:57344
	ds_read_b128 v[178:181], v208 offset:49152
	ds_read_b128 v[192:195], v208 offset:57344
	v_exp_f32_e32 v197, v68
	v_add_f32_e32 v68, 0, v170
	s_waitcnt lgkmcnt(3)
	s_setprio 1
	v_mfma_f32_32x32x16_bf16 v[98:113], v[82:85], v[142:145], 0
	v_add_f32_e32 v68, v172, v68
	v_add_f32_e32 v68, v173, v68
	v_add_f32_e32 v68, v175, v68
	v_add_f32_e32 v68, v176, v68
	v_add_f32_e32 v68, v177, v68
	v_add_f32_e32 v68, v171, v68
	v_add_f32_e32 v68, v174, v68
	s_waitcnt lgkmcnt(2)
	v_mfma_f32_32x32x16_bf16 v[82:97], v[86:89], v[142:145], 0
	v_add_f32_e32 v68, v163, v68
	v_add_f32_e32 v68, v166, v68
	v_add_f32_e32 v68, v167, v68
	v_add_f32_e32 v68, v169, v68
	v_exp_f32_e32 v80, v80
	v_add_f32_e32 v68, v162, v68
	v_exp_f32_e32 v1, v1
	s_waitcnt lgkmcnt(1)
	v_mfma_f32_32x32x16_bf16 v[98:113], v[178:181], v[138:141], v[98:113]
	v_add_f32_e32 v68, v164, v68
	v_exp_f32_e32 v2, v2
	v_add_f32_e32 v68, v165, v68
	v_exp_f32_e32 v81, v81
	v_add_f32_e32 v68, v168, v68
	v_exp_f32_e32 v78, v78
	v_add_f32_e32 v68, v80, v68
	s_waitcnt lgkmcnt(0)
	v_mfma_f32_32x32x16_bf16 v[82:97], v[192:195], v[138:141], v[82:97]
	ds_read_b128 v[178:181], v204 offset:49152
	ds_read_b128 v[192:195], v204 offset:57344
	v_exp_f32_e32 v79, v79
	v_add_f32_e32 v68, v1, v68
	v_add_f32_e32 v68, v2, v68
	v_add_f32_e32 v68, v81, v68
	v_add_f32_e32 v68, v78, v68
	v_add_f32_e32 v68, v79, v68
	s_waitcnt lgkmcnt(1)
	v_mfma_f32_32x32x16_bf16 v[98:113], v[178:181], v[134:137], v[98:113]
	v_exp_f32_e32 v223, v69
	v_cvt_pk_bf16_f32 v69, v173, v175
	v_cvt_pk_bf16_f32 v78, v78, v79
	s_waitcnt lgkmcnt(0)
	v_mfma_f32_32x32x16_bf16 v[82:97], v[192:195], v[134:137], v[82:97]
	ds_read_b128 v[178:181], v209 offset:49152
	ds_read_b128 v[192:195], v209 offset:57344
	s_waitcnt lgkmcnt(1)
	v_mfma_f32_32x32x16_bf16 v[98:113], v[178:181], v[130:133], v[98:113]
	s_waitcnt lgkmcnt(0)
	v_mfma_f32_32x32x16_bf16 v[82:97], v[192:195], v[130:133], v[82:97]
	ds_read_b128 v[178:181], v210 offset:49152
	ds_read_b128 v[192:195], v210 offset:57344
	s_waitcnt lgkmcnt(1)
	v_mfma_f32_32x32x16_bf16 v[98:113], v[178:181], v[126:129], v[98:113]
	s_waitcnt lgkmcnt(0)
	v_mfma_f32_32x32x16_bf16 v[82:97], v[192:195], v[126:129], v[82:97]
	ds_read_b128 v[178:181], v211 offset:49152
	ds_read_b128 v[192:195], v211 offset:57344
	s_waitcnt lgkmcnt(1)
	v_mfma_f32_32x32x16_bf16 v[98:113], v[178:181], v[122:125], v[98:113]
	s_waitcnt lgkmcnt(0)
	v_mfma_f32_32x32x16_bf16 v[82:97], v[192:195], v[122:125], v[82:97]
	ds_read_b128 v[178:181], v212 offset:49152
	ds_read_b128 v[192:195], v212 offset:57344
	s_waitcnt lgkmcnt(1)
	v_mfma_f32_32x32x16_bf16 v[98:113], v[178:181], v[118:121], v[98:113]
	s_waitcnt lgkmcnt(0)
	v_mfma_f32_32x32x16_bf16 v[82:97], v[192:195], v[118:121], v[82:97]
	ds_read_b128 v[178:181], v213 offset:49152
	ds_read_b128 v[192:195], v213 offset:57344
	s_waitcnt lgkmcnt(1)
	v_mfma_f32_32x32x16_bf16 v[98:113], v[178:181], v[114:117], v[98:113]
	v_exp_f32_e32 v178, v76
	v_exp_f32_e32 v179, v77
	v_exp_f32_e32 v180, v74
	v_exp_f32_e32 v181, v75
	v_add_f32_e32 v68, v178, v68
	v_add_f32_e32 v68, v179, v68
	v_add_f32_e32 v68, v180, v68
	s_waitcnt lgkmcnt(0)
	v_mfma_f32_32x32x16_bf16 v[82:97], v[192:195], v[114:117], v[82:97]
	s_setprio 0
	v_exp_f32_e32 v192, v72
	v_exp_f32_e32 v193, v73
	v_exp_f32_e32 v194, v70
	v_exp_f32_e32 v195, v71
	v_add_f32_e32 v68, v181, v68
	v_add_f32_e32 v68, v192, v68
	v_add_f32_e32 v68, v193, v68
	v_add_f32_e32 v68, v194, v68
	v_add_f32_e32 v68, v195, v68
	v_add_f32_e32 v68, v197, v68
	v_add_f32_e32 v224, v223, v68
	v_mov_b32_e32 v226, v224
	v_cvt_pk_bf16_f32 v68, v170, v172
	v_cvt_pk_bf16_f32 v70, v176, v177
	v_cvt_pk_bf16_f32 v71, v171, v174
	v_cvt_pk_bf16_f32 v72, v163, v166
	v_cvt_pk_bf16_f32 v73, v167, v169
	v_cvt_pk_bf16_f32 v74, v162, v164
	v_cvt_pk_bf16_f32 v75, v165, v168
	v_cvt_pk_bf16_f32 v76, v80, v1
	v_cvt_pk_bf16_f32 v77, v2, v81
	v_cvt_pk_bf16_f32 v79, v178, v179
	v_permlane32_swap_b32_e32 v224, v226
	v_permlane32_swap_b32_e32 v68, v70
	v_permlane32_swap_b32_e32 v69, v71
	v_permlane32_swap_b32_e32 v72, v74
	v_permlane32_swap_b32_e32 v73, v75
	v_permlane32_swap_b32_e32 v76, v78
	v_permlane32_swap_b32_e32 v77, v79
	v_cvt_pk_bf16_f32 v178, v180, v181
	v_cvt_pk_bf16_f32 v179, v192, v193
	v_cvt_pk_bf16_f32 v180, v194, v195
	v_cvt_pk_bf16_f32 v181, v197, v223
	s_nop 0
	v_permlane32_swap_b32_e32 v178, v180
	v_permlane32_swap_b32_e32 v179, v181
	s_add_i32 s8, s83, 1
	s_add_i32 s9, s83, 33
	v_mad_u64_u32 v[80:81], s[6:7], s8, v242, v[184:185]
	v_mad_u64_u32 v[166:167], s[6:7], s9, v242, v[184:185]
	global_load_dwordx4 v[162:165], v[80:81], off
	s_nop 0
	global_load_dwordx4 v[166:169], v[166:167], off
	v_mad_u64_u32 v[80:81], s[6:7], s8, v242, v[182:183]
	v_mad_u64_u32 v[174:175], s[6:7], s9, v242, v[182:183]
	global_load_dwordx4 v[170:173], v[80:81], off
	s_nop 0
	global_load_dwordx4 v[174:177], v[174:175], off
	ds_read_b64_tr_b16 v[192:193], v188
	ds_read_b64_tr_b16 v[194:195], v188 offset:2048
	ds_read_b64_tr_b16 v[232:233], v188 offset:4096
	ds_read_b64_tr_b16 v[234:235], v188 offset:6144
	ds_read_b64_tr_b16 v[236:237], v188 offset:8192
	ds_read_b64_tr_b16 v[238:239], v188 offset:10240
	ds_read_b64_tr_b16 v[244:245], v188 offset:12288
	ds_read_b64_tr_b16 v[246:247], v188 offset:14336
	s_waitcnt lgkmcnt(6)
	s_setprio 1
	v_mfma_f32_32x32x16_bf16 v[36:51], v[68:71], v[192:195], v[36:51]
	v_add_u32_e32 v1, 64, v222
	s_sub_i32 s6, s83, 64
	s_cmp_le_i32 s6, s81
	s_mov_b32 s6, 2.0
	s_mov_b32 s7, 0x40400000
	v_mov_b32_e32 v197, v196
	s_waitcnt lgkmcnt(4)
	v_mfma_f32_32x32x16_bf16 v[36:51], v[72:75], v[232:235], v[36:51]
	s_waitcnt lgkmcnt(2)
; #define LAS __attribute__((address_space(3)))
; __device__ __forceinline__ s16x4 tr_read(LAS const unsigned char* p) { return __builtin_bit_cast(s16x4, __builtin_amdgcn_ds_read_tr16_b64_v4i16((LAS v4i16_t*)p)); }
; __device__ __forceinline__ void partialSM(f32x16& p0, f32x16& p1, float& m_reg, float& mn, float& alpha, int dq, float slopeL, bool diag, bool rowmasked) {
;     const float NEG = -__builtin_inff(); const float a0 = -slopeL * (float)dq;
; #pragma unroll
;     for (int r = 0; r < 16; ++r) { const int c = (r & 3) + 8 * (r >> 2);
;         p0[r] = fmaf(p0[r], CS, fmaf(slopeL, (float)c, a0)); p1[r] = fmaf(p1[r], CS, fmaf(slopeL, (float)(c + 32), a0)); }
; template <int D0> __device__ __forceinline__ void pv_one(f32x16& od, LAS const unsigned char* vb, bf16x8 pa0, bf16x8 pa1, bf16x8 pa2, bf16x8 pa3) {
;     const s16x4 l0 = tr_read(vb + v_rd_off(D0, 0, 0)), h0 = tr_read(vb + v_rd_off(D0, 0, 1)), l1 = tr_read(vb + v_rd_off(D0, 1, 0)), h1 = tr_read(vb + v_rd_off(D0, 1, 1));
;     const s16x4 l2 = tr_read(vb + v_rd_off(D0, 2, 0)), h2 = tr_read(vb + v_rd_off(D0, 2, 1)), l3 = tr_read(vb + v_rd_off(D0, 3, 0)), h3 = tr_read(vb + v_rd_off(D0, 3, 1));
;     ...
;     od = __builtin_amdgcn_mfma_f32_32x32x16_bf16(pa0, ATT_PK(l0, h0), od, 0, 0, 0);
;     od = __builtin_amdgcn_mfma_f32_32x32x16_bf16(pa1, ATT_PK(l1, h1), od, 0, 0, 0);
;     od = __builtin_amdgcn_mfma_f32_32x32x16_bf16(pa2, ATT_PK(l2, h2), od, 0, 0, 0);
;     od = __builtin_amdgcn_mfma_f32_32x32x16_bf16(pa3, ATT_PK(l3, h3), od, 0, 0, 0);
;     ...
; }
; __device__ __forceinline__ void pv_d0(f32x16* o, LAS const unsigned char* vb, bf16x8 pa0, bf16x8 pa1, bf16x8 pa2, bf16x8 pa3) {
;     pv_one<0>(o[0], vb, pa0, pa1, pa2, pa3); pv_one<1>(o[1], vb, pa0, pa1, pa2, pa3); pv_one<2>(o[2], vb, pa0, pa1, pa2, pa3); pv_one<3>(o[3], vb, pa0, pa1, pa2, pa3);
; }
	v_mfma_f32_32x32x16_bf16 v[36:51], v[76:79], v[236:239], v[36:51]
	s_waitcnt lgkmcnt(0)
	v_mfma_f32_32x32x16_bf16 v[36:51], v[178:181], v[244:247], v[36:51]
	ds_read_b64_tr_b16 v[192:193], v188 offset:512
	ds_read_b64_tr_b16 v[194:195], v188 offset:2560
	ds_read_b64_tr_b16 v[232:233], v188 offset:4608
	ds_read_b64_tr_b16 v[234:235], v188 offset:6656
	ds_read_b64_tr_b16 v[236:237], v188 offset:8704
	ds_read_b64_tr_b16 v[238:239], v188 offset:10752
	ds_read_b64_tr_b16 v[244:245], v188 offset:12800
	ds_read_b64_tr_b16 v[246:247], v188 offset:14848
	s_waitcnt lgkmcnt(6)
	v_mfma_f32_32x32x16_bf16 v[20:35], v[68:71], v[192:195], v[20:35]
	s_waitcnt lgkmcnt(4)
	v_mfma_f32_32x32x16_bf16 v[20:35], v[72:75], v[232:235], v[20:35]
	s_waitcnt lgkmcnt(2)
	v_mfma_f32_32x32x16_bf16 v[20:35], v[76:79], v[236:239], v[20:35]
	s_waitcnt lgkmcnt(0)
	v_mfma_f32_32x32x16_bf16 v[20:35], v[178:181], v[244:247], v[20:35]
	ds_read_b64_tr_b16 v[192:193], v188 offset:1024
	ds_read_b64_tr_b16 v[194:195], v188 offset:3072
	ds_read_b64_tr_b16 v[232:233], v188 offset:5120
	ds_read_b64_tr_b16 v[234:235], v188 offset:7168
	ds_read_b64_tr_b16 v[236:237], v188 offset:9216
	ds_read_b64_tr_b16 v[238:239], v188 offset:11264
	ds_read_b64_tr_b16 v[244:245], v188 offset:13312
	ds_read_b64_tr_b16 v[246:247], v188 offset:15360
	s_waitcnt lgkmcnt(6)
	v_mfma_f32_32x32x16_bf16 v[52:67], v[68:71], v[192:195], v[52:67]
	s_waitcnt lgkmcnt(4)
	v_mfma_f32_32x32x16_bf16 v[52:67], v[72:75], v[232:235], v[52:67]
	s_waitcnt lgkmcnt(2)
	v_mfma_f32_32x32x16_bf16 v[52:67], v[76:79], v[236:239], v[52:67]
	s_waitcnt lgkmcnt(0)
	v_mfma_f32_32x32x16_bf16 v[52:67], v[178:181], v[244:247], v[52:67]
	ds_read_b64_tr_b16 v[192:193], v188 offset:1536
	ds_read_b64_tr_b16 v[194:195], v188 offset:3584
	ds_read_b64_tr_b16 v[232:233], v188 offset:5632
	ds_read_b64_tr_b16 v[234:235], v188 offset:7680
	ds_read_b64_tr_b16 v[236:237], v188 offset:9728
	ds_read_b64_tr_b16 v[238:239], v188 offset:11776
	ds_read_b64_tr_b16 v[244:245], v188 offset:13824
	ds_read_b64_tr_b16 v[246:247], v188 offset:15872
	s_waitcnt lgkmcnt(6)
	v_mfma_f32_32x32x16_bf16 v[4:19], v[68:71], v[192:195], v[4:19]
	v_cvt_f32_i32_e32 v68, v1
	v_mul_f32_e64 v2, -v196, v68
	v_fma_f32 v80, v198, s6, v2
	v_fma_f32 v81, v199, s7, v2
	s_mov_b32 s6, 0x41000000
	s_waitcnt lgkmcnt(4)
	v_mfma_f32_32x32x16_bf16 v[4:19], v[72:75], v[232:235], v[4:19]
	s_mov_b32 s7, 0x41100000
	v_fma_f32 v69, -v196, v68, v196
	v_mov_b32_e32 v68, v2
	v_fmac_f32_e32 v68, 0, v196
	v_fma_f32 v70, v198, s86, v2
	v_fma_f32 v71, v199, s87, v2
	v_pk_fma_f32 v[72:73], v[98:99], s[96:97], v[68:69] op_sel_hi:[1,0,1]
	v_pk_fma_f32 v[70:71], v[110:111], s[96:97], v[70:71] op_sel_hi:[1,0,1]
	s_waitcnt lgkmcnt(2)
	v_mfma_f32_32x32x16_bf16 v[4:19], v[76:79], v[236:239], v[4:19]
	v_fma_f32 v100, v100, s96, v80
	v_fma_f32 v101, v101, s96, v81
	v_fma_f32 v110, v196, s70, v2
	v_fma_f32 v111, v197, s71, v2
	v_fma_f32 v80, v196, s74, v2
	v_fma_f32 v81, v197, s75, v2
	v_pk_fma_f32 v[92:93], v[92:93], s[96:97], v[110:111] op_sel_hi:[1,0,1]
	v_pk_fma_f32 v[80:81], v[96:97], s[96:97], v[80:81] op_sel_hi:[1,0,1]
	s_waitcnt lgkmcnt(0)
	v_mfma_f32_32x32x16_bf16 v[4:19], v[178:181], v[244:247], v[4:19]
	s_setprio 0
	v_fma_f32 v178, v198, s6, v2
	v_fma_f32 v179, v199, s7, v2
	s_mov_b32 s6, 0x41200000
	s_mov_b32 s7, 0x41300000
	v_fma_f32 v78, v198, s6, v2
	v_fma_f32 v79, v199, s7, v2
	s_mov_b32 s6, 0x41800000
	s_mov_b32 s7, 0x41880000
	v_pk_fma_f32 v[76:77], v[198:199], s[6:7], v[2:3] op_sel_hi:[1,1,0]
	s_mov_b32 s6, 0x41900000
	s_mov_b32 s7, 0x41980000
	v_pk_fma_f32 v[74:75], v[198:199], s[6:7], v[2:3] op_sel_hi:[1,1,0]
	v_pk_fma_f32 v[180:181], v[198:199], s[88:89], v[2:3] op_sel_hi:[1,1,0]
	v_pk_fma_f32 v[74:75], v[108:109], s[96:97], v[74:75] op_sel_hi:[1,0,1]
	v_pk_fma_f32 v[68:69], v[112:113], s[96:97], v[180:181] op_sel_hi:[1,0,1]
	v_pk_fma_f32 v[76:77], v[106:107], s[96:97], v[76:77] op_sel_hi:[1,0,1]
	v_pk_fma_f32 v[78:79], v[104:105], s[96:97], v[78:79] op_sel_hi:[1,0,1]
	v_pk_fma_f32 v[98:99], v[102:103], s[96:97], v[178:179] op_sel_hi:[1,0,1]
	v_pk_fma_f32 v[102:103], v[196:197], s[90:91], v[2:3] op_sel_hi:[1,1,0]
	v_pk_fma_f32 v[104:105], v[196:197], s[92:93], v[2:3] op_sel_hi:[1,1,0]
	v_pk_fma_f32 v[106:107], v[196:197], s[94:95], v[2:3] op_sel_hi:[1,1,0]
	v_pk_fma_f32 v[108:109], v[196:197], s[68:69], v[2:3] op_sel_hi:[1,1,0]
	v_pk_fma_f32 v[112:113], v[196:197], s[72:73], v[2:3] op_sel_hi:[1,1,0]
	v_pk_fma_f32 v[178:179], v[200:201], s[76:77], v[2:3] op_sel_hi:[1,1,0]
	v_pk_fma_f32 v[94:95], v[94:95], s[96:97], v[112:113] op_sel_hi:[1,0,1]
	v_pk_fma_f32 v[90:91], v[90:91], s[96:97], v[108:109] op_sel_hi:[1,0,1]
	v_pk_fma_f32 v[88:89], v[88:89], s[96:97], v[106:107] op_sel_hi:[1,0,1]
	v_pk_fma_f32 v[86:87], v[86:87], s[96:97], v[104:105] op_sel_hi:[1,0,1]
	v_pk_fma_f32 v[84:85], v[84:85], s[96:97], v[102:103] op_sel_hi:[1,0,1]
	v_pk_fma_f32 v[82:83], v[82:83], s[96:97], v[178:179] op_sel_hi:[1,0,1]
	s_cbranch_scc1 .LBB0_824
; __device__ __forceinline__ void partialSM(f32x16& p0, f32x16& p1, float& m_reg, float& mn, float& alpha, int dq, float slopeL, bool diag, bool rowmasked) {
;     ...
;     for (int r = 0; r < 16; ++r) { const int c = (r & 3) + 8 * (r >> 2);
;         p0[r] = fmaf(p0[r], CS, fmaf(slopeL, (float)c, a0)); p1[r] = fmaf(p1[r], CS, fmaf(slopeL, (float)(c + 32), a0)); }
;     if (diag) { asm volatile("" ::: "memory");
; #pragma unroll
;         for (int r = 0; r < 16; ++r) { const int c = (r & 3) + 8 * (r >> 2); if (c > dq) p0[r] = NEG; if (c + 32 > dq) p1[r] = NEG; } }
	v_cmp_gt_i32_e64 s[64:65], 57, v1
	v_cmp_gt_i32_e64 s[66:67], 58, v1
	v_cmp_gt_i32_e64 s[62:63], 56, v1
	s_and_b64 s[64:65], s[66:67], s[64:65]
	v_cmp_gt_i32_e64 s[60:61], 51, v1
	s_and_b64 s[62:63], s[64:65], s[62:63]
	v_cmp_gt_i32_e64 s[58:59], 50, v1
	s_and_b64 s[60:61], s[62:63], s[60:61]
	v_cmp_gt_i32_e64 s[56:57], 49, v1
	s_and_b64 s[58:59], s[60:61], s[58:59]
	v_cmp_gt_i32_e64 s[54:55], 48, v1
	s_and_b64 s[56:57], s[58:59], s[56:57]
	v_cmp_gt_i32_e64 s[52:53], 43, v1
	s_and_b64 s[54:55], s[56:57], s[54:55]
	v_cmp_gt_i32_e64 s[50:51], 42, v1
	s_and_b64 s[52:53], s[54:55], s[52:53]
	v_cmp_gt_i32_e64 s[48:49], 41, v1
	s_and_b64 s[50:51], s[52:53], s[50:51]
	v_cmp_gt_i32_e64 s[46:47], 40, v1
	s_and_b64 s[48:49], s[50:51], s[48:49]
	v_cmp_gt_i32_e64 s[44:45], 35, v1
	s_and_b64 s[46:47], s[48:49], s[46:47]
	v_cmp_gt_i32_e64 s[42:43], 34, v1
	s_and_b64 s[44:45], s[46:47], s[44:45]
	v_cmp_gt_i32_e64 s[40:41], 33, v1
	s_and_b64 s[42:43], s[44:45], s[42:43]
	v_cmp_gt_i32_e64 s[38:39], 32, v1
	s_and_b64 s[40:41], s[42:43], s[40:41]
	s_and_b64 s[38:39], s[40:41], s[38:39]
	v_cmp_gt_i32_e32 vcc, 0, v1
	v_cmp_gt_i32_e64 s[6:7], 1, v1
	v_cmp_gt_i32_e64 s[8:9], 2, v1
	v_cmp_gt_i32_e64 s[10:11], 3, v1
	v_cmp_gt_i32_e64 s[14:15], 8, v1
	v_cmp_gt_i32_e64 s[16:17], 9, v1
	v_cmp_gt_i32_e64 s[18:19], 10, v1
	v_cmp_gt_i32_e64 s[20:21], 11, v1
	v_cmp_gt_i32_e64 s[22:23], 16, v1
	v_cmp_gt_i32_e64 s[24:25], 17, v1
	v_cmp_gt_i32_e64 s[26:27], 18, v1
	v_cmp_gt_i32_e64 s[28:29], 19, v1
	v_cmp_gt_i32_e64 s[30:31], 24, v1
	v_cmp_gt_i32_e64 s[34:35], 25, v1
	v_cmp_gt_i32_e64 s[36:37], 26, v1
	v_cndmask_b32_e64 v80, v80, v241, s[66:67]
	v_cndmask_b32_e64 v95, v95, v241, s[64:65]
	v_cndmask_b32_e64 v94, v94, v241, s[62:63]
	v_cndmask_b32_e64 v93, v93, v241, s[60:61]
	v_cndmask_b32_e64 v92, v92, v241, s[58:59]
	v_cndmask_b32_e64 v91, v91, v241, s[56:57]
	v_cndmask_b32_e64 v90, v90, v241, s[54:55]
	v_cndmask_b32_e64 v89, v89, v241, s[52:53]
	v_cndmask_b32_e64 v88, v88, v241, s[50:51]
	v_cndmask_b32_e64 v87, v87, v241, s[48:49]
	v_cndmask_b32_e64 v86, v86, v241, s[46:47]
	v_cndmask_b32_e64 v85, v85, v241, s[44:45]
	v_cndmask_b32_e64 v84, v84, v241, s[42:43]
	v_cndmask_b32_e64 v83, v83, v241, s[40:41]
	v_cndmask_b32_e64 v82, v82, v241, s[38:39]
	v_cmp_gt_i32_e64 s[38:39], 27, v1
	v_cmp_gt_i32_e64 s[40:41], 59, v1
	s_and_saveexec_b64 s[12:13], s[40:41]
	v_mov_b32_e32 v81, s85
	s_or_b64 exec, exec, s[12:13]
	s_and_b64 s[36:37], s[38:39], s[36:37]
	s_and_b64 s[34:35], s[36:37], s[34:35]
	s_and_b64 s[30:31], s[34:35], s[30:31]
	s_and_b64 s[28:29], s[30:31], s[28:29]
	s_and_b64 s[26:27], s[28:29], s[26:27]
	s_and_b64 s[24:25], s[26:27], s[24:25]
	s_and_b64 s[22:23], s[24:25], s[22:23]
	s_and_b64 s[20:21], s[22:23], s[20:21]
	s_and_b64 s[18:19], s[20:21], s[18:19]
	s_and_b64 s[16:17], s[18:19], s[16:17]
	s_and_b64 s[14:15], s[16:17], s[14:15]
	s_and_b64 s[10:11], s[14:15], s[10:11]
	s_and_b64 s[8:9], s[10:11], s[8:9]
	s_and_b64 s[6:7], s[8:9], s[6:7]
	s_and_b64 vcc, s[6:7], vcc
	v_cndmask_b32_e64 v68, v68, v241, s[36:37]
	v_cndmask_b32_e64 v71, v71, v241, s[34:35]
	v_cndmask_b32_e64 v70, v70, v241, s[30:31]
	v_cndmask_b32_e64 v75, v75, v241, s[28:29]
	v_cndmask_b32_e64 v74, v74, v241, s[26:27]
	v_cndmask_b32_e64 v77, v77, v241, s[24:25]
	v_cndmask_b32_e64 v76, v76, v241, s[22:23]
	v_cndmask_b32_e64 v79, v79, v241, s[20:21]
	v_cndmask_b32_e64 v78, v78, v241, s[18:19]
	v_cndmask_b32_e64 v99, v99, v241, s[16:17]
	v_cndmask_b32_e64 v98, v98, v241, s[14:15]
	v_cndmask_b32_e64 v101, v101, v241, s[10:11]
	v_cndmask_b32_e64 v100, v100, v241, s[8:9]
	v_cndmask_b32_e64 v73, v73, v241, s[6:7]
	v_cndmask_b32_e32 v72, v72, v241, vcc
	v_cndmask_b32_e64 v69, v69, v241, s[38:39]

; __device__ __forceinline__ void qkt(f32x16& p0, f32x16& p1, LAS const unsigned char* Ks, const bf16x8* qr, int r32, int hi) {
;     p0 = f32x16{}; p1 = f32x16{};
; #pragma unroll
;     for (int d0 = 0; d0 < 8; ++d0) { const int cb = (d0 * 16 + hi * 8) * 2;
;         const bf16x8 b0 = *(LAS const bf16x8*)(Ks + ATT_KSWZ(r32, cb));
;         const bf16x8 b1 = *(LAS const bf16x8*)(Ks + ATT_KSWZ(32 + r32, cb));
;         p0 = __builtin_amdgcn_mfma_f32_32x32x16_bf16(b0, qr[d0], p0, 0, 0, 0);
;         p1 = __builtin_amdgcn_mfma_f32_32x32x16_bf16(b1, qr[d0], p1, 0, 0, 0); }
; }
; __device__ __forceinline__ void partialSM(f32x16& p0, f32x16& p1, float& m_reg, float& mn, float& alpha, int dq, float slopeL, bool diag, bool rowmasked) {
;     const float NEG = -__builtin_inff(); const float a0 = -slopeL * (float)dq;
; #pragma unroll
;     for (int r = 0; r < 16; ++r) { const int c = (r & 3) + 8 * (r >> 2);
;         p0[r] = fmaf(p0[r], CS, fmaf(slopeL, (float)c, a0)); p1[r] = fmaf(p1[r], CS, fmaf(slopeL, (float)(c + 32), a0)); }
;     if (diag) { asm volatile("" ::: "memory");
; #pragma unroll
;         for (int r = 0; r < 16; ++r) { const int c = (r & 3) + 8 * (r >> 2); if (c > dq) p0[r] = NEG; if (c + 32 > dq) p1[r] = NEG; } }
;     if (rowmasked) {
; #pragma unroll
;         for (int r = 0; r < 16; ++r) { p0[r] = NEG; p1[r] = NEG; } }
;     float pmax = p0[0];
; #pragma unroll
;     for (int r = 1; r < 16; ++r) pmax = fmaxf(pmax, p0[r]);
; #pragma unroll
;     for (int r = 0; r < 16; ++r) pmax = fmaxf(pmax, p1[r]);
;     { auto rr = __builtin_amdgcn_permlane32_swap(__float_as_uint(pmax), __float_as_uint(pmax), false, false);
;       pmax = fmaxf(__uint_as_float(rr[0]), __uint_as_float(rr[1])); }
;     if (__builtin_expect(__all(pmax - m_reg <= THRL), 1)) { mn = m_reg; alpha = 1.f; }
;     else { mn = fmaxf(m_reg, pmax); alpha = __builtin_amdgcn_exp2f(m_reg - mn); m_reg = mn; }
; #pragma unroll
;     for (int r = 0; r < 16; ++r) { p0[r] = p0[r] - mn; p1[r] = p1[r] - mn; }
; #pragma unroll
;     for (int r = 0; r < 16; ++r) p0[r] = __builtin_amdgcn_exp2f(p0[r]);
; }
; __device__ __forceinline__ void finishSM(f32x16& p0, f32x16& p1, float alpha, float& l_reg, bf16x8& pa0, bf16x8& pa1, bf16x8& pa2, bf16x8& pa3) {
; #pragma unroll
;     for (int r = 0; r < 16; ++r) p1[r] = __builtin_amdgcn_exp2f(p1[r]);
;     float ps = 0;
; #pragma unroll
.LBB0_828:
	v_cndmask_b32_e64 v1, v1, v220, s[6:7]
	v_sub_f32_e32 v2, v72, v1
	v_sub_f32_e32 v72, v73, v1
	v_sub_f32_e32 v73, v100, v1
	v_sub_f32_e32 v96, v101, v1
	v_sub_f32_e32 v97, v98, v1
	v_sub_f32_e32 v98, v99, v1
	v_sub_f32_e32 v78, v78, v1
	v_sub_f32_e32 v79, v79, v1
	v_sub_f32_e32 v76, v76, v1
	v_sub_f32_e32 v77, v77, v1
	v_sub_f32_e32 v74, v74, v1
	v_sub_f32_e32 v75, v75, v1
	v_sub_f32_e32 v71, v71, v1
	v_sub_f32_e32 v68, v68, v1
	v_sub_f32_e32 v69, v69, v1
	v_exp_f32_e32 v100, v2
	v_exp_f32_e32 v101, v72
	v_exp_f32_e32 v102, v73
	v_exp_f32_e32 v178, v96
	v_exp_f32_e32 v179, v97
	v_exp_f32_e32 v180, v98
	v_exp_f32_e32 v103, v78
	v_exp_f32_e32 v111, v79
	v_exp_f32_e32 v104, v76
	v_exp_f32_e32 v105, v77
	v_exp_f32_e32 v109, v74
	v_exp_f32_e32 v110, v75
	v_exp_f32_e32 v106, v71
	v_exp_f32_e32 v107, v68
	v_exp_f32_e32 v108, v69
	v_sub_f32_e32 v70, v70, v1
	v_sub_f32_e32 v113, v82, v1
	v_sub_f32_e32 v181, v83, v1
	v_sub_f32_e32 v223, v86, v1
	v_exp_f32_e32 v2, v70
	v_sub_f32_e32 v197, v84, v1
	v_sub_f32_e32 v220, v85, v1
	v_sub_f32_e32 v228, v87, v1
	v_sub_f32_e32 v230, v88, v1
	v_sub_f32_e32 v236, v89, v1
	v_sub_f32_e32 v237, v90, v1
	v_sub_f32_e32 v238, v91, v1
	v_sub_f32_e32 v239, v92, v1
	v_sub_f32_e32 v240, v93, v1
	v_sub_f32_e32 v244, v94, v1
	v_sub_f32_e32 v245, v95, v1
	v_sub_f32_e32 v246, v80, v1
	v_sub_f32_e32 v247, v81, v1
	s_waitcnt lgkmcnt(0)
	s_barrier
	ds_read_b128 v[68:71], v206 offset:32768
	ds_read_b128 v[72:75], v206 offset:40960
	ds_read_b128 v[192:195], v208 offset:32768
	ds_read_b128 v[232:235], v208 offset:40960
	v_exp_f32_e32 v181, v181
	s_waitcnt lgkmcnt(3)
	s_setprio 1
	v_mfma_f32_32x32x16_bf16 v[84:99], v[68:71], v[142:145], 0
	s_waitcnt lgkmcnt(2)
	v_mfma_f32_32x32x16_bf16 v[68:83], v[72:75], v[142:145], 0
	s_waitcnt lgkmcnt(1)
	v_mfma_f32_32x32x16_bf16 v[84:99], v[192:195], v[138:141], v[84:99]
	s_waitcnt lgkmcnt(0)
	v_mfma_f32_32x32x16_bf16 v[68:83], v[232:235], v[138:141], v[68:83]
	ds_read_b128 v[192:195], v204 offset:32768
	ds_read_b128 v[232:235], v204 offset:40960
	s_waitcnt lgkmcnt(1)
	v_mfma_f32_32x32x16_bf16 v[84:99], v[192:195], v[134:137], v[84:99]
	s_waitcnt lgkmcnt(0)
	v_mfma_f32_32x32x16_bf16 v[68:83], v[232:235], v[134:137], v[68:83]
	ds_read_b128 v[192:195], v209 offset:32768
	ds_read_b128 v[232:235], v209 offset:40960
	s_waitcnt lgkmcnt(1)
	v_mfma_f32_32x32x16_bf16 v[84:99], v[192:195], v[130:133], v[84:99]
	s_waitcnt lgkmcnt(0)
	v_mfma_f32_32x32x16_bf16 v[68:83], v[232:235], v[130:133], v[68:83]
	ds_read_b128 v[192:195], v210 offset:32768
	ds_read_b128 v[232:235], v210 offset:40960
	s_waitcnt lgkmcnt(1)
	v_mfma_f32_32x32x16_bf16 v[84:99], v[192:195], v[126:129], v[84:99]
	s_waitcnt lgkmcnt(0)
	v_mfma_f32_32x32x16_bf16 v[68:83], v[232:235], v[126:129], v[68:83]
	ds_read_b128 v[192:195], v211 offset:32768
	ds_read_b128 v[232:235], v211 offset:40960
	s_waitcnt lgkmcnt(1)
	v_mfma_f32_32x32x16_bf16 v[84:99], v[192:195], v[122:125], v[84:99]
	s_waitcnt lgkmcnt(0)
	v_mfma_f32_32x32x16_bf16 v[68:83], v[232:235], v[122:125], v[68:83]
	ds_read_b128 v[192:195], v212 offset:32768
	ds_read_b128 v[232:235], v212 offset:40960
	s_waitcnt lgkmcnt(1)
	v_mfma_f32_32x32x16_bf16 v[84:99], v[192:195], v[118:121], v[84:99]
	s_waitcnt lgkmcnt(0)
	v_mfma_f32_32x32x16_bf16 v[68:83], v[232:235], v[118:121], v[68:83]
	ds_read_b128 v[192:195], v213 offset:32768
	ds_read_b128 v[232:235], v213 offset:40960
	s_waitcnt lgkmcnt(1)
	v_mfma_f32_32x32x16_bf16 v[84:99], v[192:195], v[114:117], v[84:99]
	s_setprio 0
	v_exp_f32_e32 v192, v113
	v_add_f32_e32 v113, 0, v100
	v_add_f32_e32 v113, v101, v113
	v_add_f32_e32 v113, v102, v113
	v_add_f32_e32 v113, v178, v113
	v_add_f32_e32 v113, v179, v113
	v_add_f32_e32 v113, v180, v113
	v_add_f32_e32 v113, v103, v113
	v_add_f32_e32 v113, v111, v113
	v_add_f32_e32 v113, v104, v113
	v_add_f32_e32 v113, v105, v113
	v_add_f32_e32 v113, v109, v113
	v_add_f32_e32 v113, v110, v113
	v_add_f32_e32 v113, v2, v113
	v_add_f32_e32 v113, v106, v113
	v_exp_f32_e32 v193, v197
	v_add_f32_e32 v113, v107, v113
	v_exp_f32_e32 v194, v220
	v_add_f32_e32 v113, v108, v113
	v_exp_f32_e32 v195, v223
	v_add_f32_e32 v113, v192, v113
	v_exp_f32_e32 v197, v228
	v_add_f32_e32 v113, v181, v113
	v_exp_f32_e32 v220, v230
	v_add_f32_e32 v113, v193, v113
	v_exp_f32_e32 v228, v236
	v_add_f32_e32 v113, v194, v113
	v_exp_f32_e32 v230, v237
	v_add_f32_e32 v113, v195, v113
	s_waitcnt lgkmcnt(0)
	s_setprio 1
	v_mfma_f32_32x32x16_bf16 v[68:83], v[232:235], v[114:117], v[68:83]
	s_setprio 0
	v_exp_f32_e32 v232, v238
	v_add_f32_e32 v113, v197, v113
	v_exp_f32_e32 v233, v239
	v_add_f32_e32 v113, v220, v113
	v_exp_f32_e32 v234, v240
	v_add_f32_e32 v113, v228, v113
	v_exp_f32_e32 v235, v244
	v_add_f32_e32 v113, v230, v113
	v_exp_f32_e32 v236, v245
	v_add_f32_e32 v113, v232, v113
	v_exp_f32_e32 v237, v246
	v_add_f32_e32 v113, v233, v113
	v_exp_f32_e32 v238, v247
	v_add_f32_e32 v113, v234, v113
	v_add_f32_e32 v113, v235, v113
	v_add_f32_e32 v113, v236, v113
	v_add_f32_e32 v113, v237, v113
	v_add_f32_e32 v113, v238, v113
	v_mov_b32_e32 v223, v113
	v_cvt_pk_bf16_f32 v100, v100, v101
	v_cvt_pk_bf16_f32 v101, v102, v178
	v_cvt_pk_bf16_f32 v102, v179, v180
	v_cvt_pk_bf16_f32 v103, v103, v111
	v_cvt_pk_bf16_f32 v104, v104, v105
	v_cvt_pk_bf16_f32 v105, v109, v110
	v_cvt_pk_bf16_f32 v106, v2, v106
	v_cvt_pk_bf16_f32 v107, v107, v108
	v_cvt_pk_bf16_f32 v108, v192, v181
	v_cvt_pk_bf16_f32 v109, v193, v194
	v_cvt_pk_bf16_f32 v110, v195, v197
	v_cvt_pk_bf16_f32 v111, v220, v228
	v_cvt_pk_bf16_f32 v178, v230, v232
	v_cvt_pk_bf16_f32 v179, v233, v234
	v_cvt_pk_bf16_f32 v180, v235, v236
	v_cvt_pk_bf16_f32 v181, v237, v238
	v_permlane32_swap_b32_e32 v113, v223
	v_permlane32_swap_b32_e32 v100, v102
	v_permlane32_swap_b32_e32 v101, v103
	v_permlane32_swap_b32_e32 v104, v106
	v_permlane32_swap_b32_e32 v105, v107
	v_permlane32_swap_b32_e32 v108, v110
	v_permlane32_swap_b32_e32 v109, v111
	v_permlane32_swap_b32_e32 v178, v180
	v_permlane32_swap_b32_e32 v179, v181
	s_cmp_ge_i32 s84, s82
	s_cselect_b64 s[12:13], -1, 0
	s_and_b64 vcc, exec, s[12:13]
	s_cbranch_vccnz .LBB0_830
	s_add_i32 s8, s83, 0x41
	s_add_i32 s9, s83, 0x61
	v_mad_u64_u32 v[146:147], s[6:7], s8, v242, v[184:185]
	v_mad_u64_u32 v[150:151], s[6:7], s9, v242, v[184:185]
	v_mad_u64_u32 v[154:155], s[6:7], s8, v242, v[182:183]
	v_mad_u64_u32 v[158:159], s[6:7], s9, v242, v[182:183]
	global_load_dwordx4 v[146:149], v[146:147], off
	s_nop 0
	global_load_dwordx4 v[150:153], v[150:151], off
	s_nop 0
	global_load_dwordx4 v[154:157], v[154:155], off
	s_nop 0
	global_load_dwordx4 v[158:161], v[158:159], off
; #define LAS __attribute__((address_space(3)))
; __device__ __forceinline__ s16x4 tr_read(LAS const unsigned char* p) { return __builtin_bit_cast(s16x4, __builtin_amdgcn_ds_read_tr16_b64_v4i16((LAS v4i16_t*)p)); }
; __device__ __forceinline__ void partialSM(f32x16& p0, f32x16& p1, float& m_reg, float& mn, float& alpha, int dq, float slopeL, bool diag, bool rowmasked) {
;     const float NEG = -__builtin_inff(); const float a0 = -slopeL * (float)dq;
; #pragma unroll
;     for (int r = 0; r < 16; ++r) { const int c = (r & 3) + 8 * (r >> 2);
;         p0[r] = fmaf(p0[r], CS, fmaf(slopeL, (float)c, a0)); p1[r] = fmaf(p1[r], CS, fmaf(slopeL, (float)(c + 32), a0)); }
; template <int D0> __device__ __forceinline__ void pv_one(f32x16& od, LAS const unsigned char* vb, bf16x8 pa0, bf16x8 pa1, bf16x8 pa2, bf16x8 pa3) {
;     const s16x4 l0 = tr_read(vb + v_rd_off(D0, 0, 0)), h0 = tr_read(vb + v_rd_off(D0, 0, 1)), l1 = tr_read(vb + v_rd_off(D0, 1, 0)), h1 = tr_read(vb + v_rd_off(D0, 1, 1));
;     const s16x4 l2 = tr_read(vb + v_rd_off(D0, 2, 0)), h2 = tr_read(vb + v_rd_off(D0, 2, 1)), l3 = tr_read(vb + v_rd_off(D0, 3, 0)), h3 = tr_read(vb + v_rd_off(D0, 3, 1));
;     ...
;     od = __builtin_amdgcn_mfma_f32_32x32x16_bf16(pa0, ATT_PK(l0, h0), od, 0, 0, 0);
;     od = __builtin_amdgcn_mfma_f32_32x32x16_bf16(pa1, ATT_PK(l1, h1), od, 0, 0, 0);
;     od = __builtin_amdgcn_mfma_f32_32x32x16_bf16(pa2, ATT_PK(l2, h2), od, 0, 0, 0);
;     od = __builtin_amdgcn_mfma_f32_32x32x16_bf16(pa3, ATT_PK(l3, h3), od, 0, 0, 0);
;     ...
; }
; __device__ __forceinline__ void pv_d0(f32x16* o, LAS const unsigned char* vb, bf16x8 pa0, bf16x8 pa1, bf16x8 pa2, bf16x8 pa3) {
;     pv_one<0>(o[0], vb, pa0, pa1, pa2, pa3); pv_one<1>(o[1], vb, pa0, pa1, pa2, pa3); pv_one<2>(o[2], vb, pa0, pa1, pa2, pa3); pv_one<3>(o[3], vb, pa0, pa1, pa2, pa3);
; }
.LBB0_830:
	ds_read_b64_tr_b16 v[192:193], v188 offset:16384
	ds_read_b64_tr_b16 v[194:195], v188 offset:18432
	ds_read_b64_tr_b16 v[232:233], v188 offset:20480
	ds_read_b64_tr_b16 v[234:235], v188 offset:22528
	ds_read_b64_tr_b16 v[236:237], v188 offset:24576
	ds_read_b64_tr_b16 v[238:239], v188 offset:26624
	ds_read_b64_tr_b16 v[244:245], v188 offset:28672
	ds_read_b64_tr_b16 v[246:247], v188 offset:30720
	s_waitcnt lgkmcnt(6)
	s_setprio 1
	v_mfma_f32_32x32x16_bf16 v[36:51], v[100:103], v[192:195], v[36:51]
	s_mov_b32 s6, 2.0
	s_mov_b32 s7, 0x40400000
	v_mov_b32_e32 v197, v196
	s_cmp_le_i32 s83, s81
	s_waitcnt lgkmcnt(4)
	v_mfma_f32_32x32x16_bf16 v[36:51], v[104:107], v[232:235], v[36:51]
	s_waitcnt lgkmcnt(2)
	v_mfma_f32_32x32x16_bf16 v[36:51], v[108:111], v[236:239], v[36:51]
	s_waitcnt lgkmcnt(0)
	v_mfma_f32_32x32x16_bf16 v[36:51], v[178:181], v[244:247], v[36:51]
	ds_read_b64_tr_b16 v[192:193], v188 offset:16896
	ds_read_b64_tr_b16 v[194:195], v188 offset:18944
	ds_read_b64_tr_b16 v[232:233], v188 offset:20992
	ds_read_b64_tr_b16 v[234:235], v188 offset:23040
	ds_read_b64_tr_b16 v[236:237], v188 offset:25088
	ds_read_b64_tr_b16 v[238:239], v188 offset:27136
	ds_read_b64_tr_b16 v[244:245], v188 offset:29184
	ds_read_b64_tr_b16 v[246:247], v188 offset:31232
	s_waitcnt lgkmcnt(6)
	v_mfma_f32_32x32x16_bf16 v[20:35], v[100:103], v[192:195], v[20:35]
	s_waitcnt lgkmcnt(4)
	v_mfma_f32_32x32x16_bf16 v[20:35], v[104:107], v[232:235], v[20:35]
	s_waitcnt lgkmcnt(2)
	v_mfma_f32_32x32x16_bf16 v[20:35], v[108:111], v[236:239], v[20:35]
	s_waitcnt lgkmcnt(0)
	v_mfma_f32_32x32x16_bf16 v[20:35], v[178:181], v[244:247], v[20:35]
	ds_read_b64_tr_b16 v[192:193], v188 offset:17408
	ds_read_b64_tr_b16 v[194:195], v188 offset:19456
	ds_read_b64_tr_b16 v[232:233], v188 offset:21504
	ds_read_b64_tr_b16 v[234:235], v188 offset:23552
	ds_read_b64_tr_b16 v[236:237], v188 offset:25600
	ds_read_b64_tr_b16 v[238:239], v188 offset:27648
	ds_read_b64_tr_b16 v[244:245], v188 offset:29696
	ds_read_b64_tr_b16 v[246:247], v188 offset:31744
	s_waitcnt lgkmcnt(6)
	v_mfma_f32_32x32x16_bf16 v[52:67], v[100:103], v[192:195], v[52:67]
	s_waitcnt lgkmcnt(4)
	v_mfma_f32_32x32x16_bf16 v[52:67], v[104:107], v[232:235], v[52:67]
	s_waitcnt lgkmcnt(2)
	v_mfma_f32_32x32x16_bf16 v[52:67], v[108:111], v[236:239], v[52:67]
	s_waitcnt lgkmcnt(0)
	v_mfma_f32_32x32x16_bf16 v[52:67], v[178:181], v[244:247], v[52:67]
	ds_read_b64_tr_b16 v[192:193], v188 offset:17920
	ds_read_b64_tr_b16 v[194:195], v188 offset:19968
	ds_read_b64_tr_b16 v[232:233], v188 offset:22016
	ds_read_b64_tr_b16 v[234:235], v188 offset:24064
	ds_read_b64_tr_b16 v[236:237], v188 offset:26112
	ds_read_b64_tr_b16 v[238:239], v188 offset:28160
	ds_read_b64_tr_b16 v[244:245], v188 offset:30208
	ds_read_b64_tr_b16 v[246:247], v188 offset:32256
	s_waitcnt lgkmcnt(6)
	v_mfma_f32_32x32x16_bf16 v[4:19], v[100:103], v[192:195], v[4:19]
	v_cvt_f32_i32_e32 v100, v222
	v_mul_f32_e64 v2, -v196, v100
	v_fma_f32 v102, v198, s6, v2
	v_fma_f32 v103, v199, s7, v2
	s_mov_b32 s6, 0x41000000
	s_waitcnt lgkmcnt(4)
	v_mfma_f32_32x32x16_bf16 v[4:19], v[104:107], v[232:235], v[4:19]
	s_mov_b32 s7, 0x41100000
	v_fma_f32 v104, v198, s6, v2
	v_fma_f32 v105, v199, s7, v2
	s_mov_b32 s6, 0x41200000
	s_mov_b32 s7, 0x41300000
	v_pk_fma_f32 v[106:107], v[198:199], s[6:7], v[2:3] op_sel_hi:[1,1,0]
	s_mov_b32 s6, 0x41800000
	s_mov_b32 s7, 0x41880000
	s_waitcnt lgkmcnt(2)
	v_mfma_f32_32x32x16_bf16 v[4:19], v[108:111], v[236:239], v[4:19]
	v_fma_f32 v108, v198, s6, v2
	v_fma_f32 v109, v199, s7, v2
	s_mov_b32 s6, 0x41900000
	v_fma_f32 v101, -v196, v100, v196
	v_mov_b32_e32 v100, v2
	s_mov_b32 s7, 0x41980000
	v_fmac_f32_e32 v100, 0, v196
	v_pk_fma_f32 v[110:111], v[198:199], s[6:7], v[2:3] op_sel_hi:[1,1,0]
	s_waitcnt lgkmcnt(0)
	v_mfma_f32_32x32x16_bf16 v[4:19], v[178:181], v[244:247], v[4:19]
	s_setprio 0
	v_fma_f32 v178, v198, s86, v2
	v_fma_f32 v179, v199, s87, v2
	v_fma_f32 v180, v198, s88, v2
	v_fma_f32 v181, v199, s89, v2
	v_fma_f32 v96, v96, s96, v178
	v_fma_f32 v97, v97, s96, v179
	v_pk_fma_f32 v[98:99], v[98:99], s[96:97], v[180:181] op_sel_hi:[1,0,1]
	v_pk_fma_f32 v[94:95], v[94:95], s[96:97], v[110:111] op_sel_hi:[1,0,1]
	v_pk_fma_f32 v[92:93], v[92:93], s[96:97], v[108:109] op_sel_hi:[1,0,1]
	v_pk_fma_f32 v[90:91], v[90:91], s[96:97], v[106:107] op_sel_hi:[1,0,1]
	v_pk_fma_f32 v[88:89], v[88:89], s[96:97], v[104:105] op_sel_hi:[1,0,1]
	v_pk_fma_f32 v[86:87], v[86:87], s[96:97], v[102:103] op_sel_hi:[1,0,1]
	v_pk_fma_f32 v[84:85], v[84:85], s[96:97], v[100:101] op_sel_hi:[1,0,1]
	v_pk_fma_f32 v[106:107], v[196:197], s[90:91], v[2:3] op_sel_hi:[1,1,0]
	v_pk_fma_f32 v[104:105], v[196:197], s[92:93], v[2:3] op_sel_hi:[1,1,0]
	v_pk_fma_f32 v[102:103], v[196:197], s[94:95], v[2:3] op_sel_hi:[1,1,0]
	v_pk_fma_f32 v[108:109], v[196:197], s[68:69], v[2:3] op_sel_hi:[1,1,0]
	v_pk_fma_f32 v[110:111], v[196:197], s[70:71], v[2:3] op_sel_hi:[1,1,0]
	v_pk_fma_f32 v[178:179], v[196:197], s[72:73], v[2:3] op_sel_hi:[1,1,0]
	v_pk_fma_f32 v[100:101], v[196:197], s[74:75], v[2:3] op_sel_hi:[1,1,0]
	v_pk_fma_f32 v[180:181], v[200:201], s[76:77], v[2:3] op_sel_hi:[1,1,0]
	v_pk_fma_f32 v[100:101], v[82:83], s[96:97], v[100:101] op_sel_hi:[1,0,1]
	v_pk_fma_f32 v[80:81], v[80:81], s[96:97], v[178:179] op_sel_hi:[1,0,1]
	v_pk_fma_f32 v[78:79], v[78:79], s[96:97], v[110:111] op_sel_hi:[1,0,1]
	v_pk_fma_f32 v[76:77], v[76:77], s[96:97], v[108:109] op_sel_hi:[1,0,1]
	v_pk_fma_f32 v[102:103], v[74:75], s[96:97], v[102:103] op_sel_hi:[1,0,1]
	v_pk_fma_f32 v[104:105], v[72:73], s[96:97], v[104:105] op_sel_hi:[1,0,1]
	v_pk_fma_f32 v[106:107], v[70:71], s[96:97], v[106:107] op_sel_hi:[1,0,1]
	v_pk_fma_f32 v[82:83], v[68:69], s[96:97], v[180:181] op_sel_hi:[1,0,1]
	s_cbranch_scc1 .LBB0_834
; __device__ __forceinline__ void partialSM(f32x16& p0, f32x16& p1, float& m_reg, float& mn, float& alpha, int dq, float slopeL, bool diag, bool rowmasked) {
;     ...
;     for (int r = 0; r < 16; ++r) { const int c = (r & 3) + 8 * (r >> 2);
;         p0[r] = fmaf(p0[r], CS, fmaf(slopeL, (float)c, a0)); p1[r] = fmaf(p1[r], CS, fmaf(slopeL, (float)(c + 32), a0)); }
;     if (diag) { asm volatile("" ::: "memory");
; #pragma unroll
;         for (int r = 0; r < 16; ++r) { const int c = (r & 3) + 8 * (r >> 2); if (c > dq) p0[r] = NEG; if (c + 32 > dq) p1[r] = NEG; } }
	v_cmp_gt_i32_e64 s[64:65], 57, v222
	v_cmp_gt_i32_e64 s[66:67], 58, v222
	v_cmp_gt_i32_e64 s[62:63], 56, v222
	s_and_b64 s[64:65], s[66:67], s[64:65]
	v_cmp_gt_i32_e64 s[60:61], 51, v222
	s_and_b64 s[62:63], s[64:65], s[62:63]
	v_cmp_gt_i32_e64 s[58:59], 50, v222
	s_and_b64 s[60:61], s[62:63], s[60:61]
	v_cmp_gt_i32_e64 s[56:57], 49, v222
	s_and_b64 s[58:59], s[60:61], s[58:59]
	v_cmp_gt_i32_e64 s[54:55], 48, v222
	s_and_b64 s[56:57], s[58:59], s[56:57]
	v_cmp_gt_i32_e64 s[52:53], 43, v222
	s_and_b64 s[54:55], s[56:57], s[54:55]
	v_cmp_gt_i32_e64 s[50:51], 42, v222
	s_and_b64 s[52:53], s[54:55], s[52:53]
	v_cmp_gt_i32_e64 s[48:49], 41, v222
	s_and_b64 s[50:51], s[52:53], s[50:51]
	v_cmp_gt_i32_e64 s[46:47], 40, v222
	s_and_b64 s[48:49], s[50:51], s[48:49]
	v_cmp_gt_i32_e64 s[44:45], 35, v222
	s_and_b64 s[46:47], s[48:49], s[46:47]
	v_cmp_gt_i32_e64 s[42:43], 34, v222
	s_and_b64 s[44:45], s[46:47], s[44:45]
	v_cmp_gt_i32_e64 s[40:41], 33, v222
	s_and_b64 s[42:43], s[44:45], s[42:43]
	v_cmp_gt_i32_e64 s[38:39], 32, v222
	s_and_b64 s[40:41], s[42:43], s[40:41]
	s_and_b64 s[38:39], s[40:41], s[38:39]
	v_cmp_gt_i32_e32 vcc, 0, v222
	v_cmp_gt_i32_e64 s[6:7], 1, v222
	v_cmp_gt_i32_e64 s[8:9], 2, v222
	v_cmp_gt_i32_e64 s[10:11], 3, v222
	v_cmp_gt_i32_e64 s[14:15], 8, v222
	v_cmp_gt_i32_e64 s[16:17], 9, v222
	v_cmp_gt_i32_e64 s[18:19], 10, v222
	v_cmp_gt_i32_e64 s[20:21], 11, v222
	v_cmp_gt_i32_e64 s[22:23], 16, v222
	v_cmp_gt_i32_e64 s[24:25], 17, v222
	v_cmp_gt_i32_e64 s[26:27], 18, v222
	v_cmp_gt_i32_e64 s[28:29], 19, v222
	v_cmp_gt_i32_e64 s[30:31], 24, v222
	v_cmp_gt_i32_e64 s[34:35], 25, v222
	v_cmp_gt_i32_e64 s[36:37], 26, v222
	v_cndmask_b32_e64 v100, v100, v241, s[66:67]
	v_cndmask_b32_e64 v81, v81, v241, s[64:65]
	v_cndmask_b32_e64 v80, v80, v241, s[62:63]
	v_cndmask_b32_e64 v79, v79, v241, s[60:61]
	v_cndmask_b32_e64 v78, v78, v241, s[58:59]
	v_cndmask_b32_e64 v77, v77, v241, s[56:57]
	v_cndmask_b32_e64 v76, v76, v241, s[54:55]
	v_cndmask_b32_e64 v103, v103, v241, s[52:53]
	v_cndmask_b32_e64 v102, v102, v241, s[50:51]
	v_cndmask_b32_e64 v105, v105, v241, s[48:49]
	v_cndmask_b32_e64 v104, v104, v241, s[46:47]
	v_cndmask_b32_e64 v107, v107, v241, s[44:45]
	v_cndmask_b32_e64 v106, v106, v241, s[42:43]
	v_cndmask_b32_e64 v83, v83, v241, s[40:41]
	v_cndmask_b32_e64 v82, v82, v241, s[38:39]
	v_cmp_gt_i32_e64 s[38:39], 27, v222
	v_cmp_gt_i32_e64 s[40:41], 59, v222
	s_and_saveexec_b64 s[42:43], s[40:41]
	v_mov_b32_e32 v101, s85
	s_or_b64 exec, exec, s[42:43]
	s_and_b64 s[36:37], s[38:39], s[36:37]
	s_and_b64 s[34:35], s[36:37], s[34:35]
	s_and_b64 s[30:31], s[34:35], s[30:31]
	s_and_b64 s[28:29], s[30:31], s[28:29]
	s_and_b64 s[26:27], s[28:29], s[26:27]
	s_and_b64 s[24:25], s[26:27], s[24:25]
	s_and_b64 s[22:23], s[24:25], s[22:23]
	s_and_b64 s[20:21], s[22:23], s[20:21]
	s_and_b64 s[18:19], s[20:21], s[18:19]
	s_and_b64 s[16:17], s[18:19], s[16:17]
	s_and_b64 s[14:15], s[16:17], s[14:15]
	s_and_b64 s[10:11], s[14:15], s[10:11]
	s_and_b64 s[8:9], s[10:11], s[8:9]
	s_and_b64 s[6:7], s[8:9], s[6:7]
	s_and_b64 vcc, s[6:7], vcc
	v_cndmask_b32_e64 v98, v98, v241, s[36:37]
	v_cndmask_b32_e64 v97, v97, v241, s[34:35]
	v_cndmask_b32_e64 v96, v96, v241, s[30:31]
	v_cndmask_b32_e64 v95, v95, v241, s[28:29]
	v_cndmask_b32_e64 v94, v94, v241, s[26:27]
	v_cndmask_b32_e64 v93, v93, v241, s[24:25]
	v_cndmask_b32_e64 v92, v92, v241, s[22:23]
	v_cndmask_b32_e64 v91, v91, v241, s[20:21]
	v_cndmask_b32_e64 v90, v90, v241, s[18:19]
	v_cndmask_b32_e64 v89, v89, v241, s[16:17]
	v_cndmask_b32_e64 v88, v88, v241, s[14:15]
	v_cndmask_b32_e64 v87, v87, v241, s[10:11]
	v_cndmask_b32_e64 v86, v86, v241, s[8:9]
	v_cndmask_b32_e64 v85, v85, v241, s[6:7]
	v_cndmask_b32_e32 v84, v84, v241, vcc
	v_cndmask_b32_e64 v99, v99, v241, s[38:39]
